# filler s_nop slots deleted from the four attention loops (hazard distances re-checked with a table-driven checker)
# speedup vs baseline: 1.0122x; 1.0122x over previous
; DI void attn_unit_d8(unsigned char* lds, const AttnArgs& a) {
;     ...
;     auto expsum = [&](f32x16& sc, f32x4& l) __attribute__((always_inline)) {
; #pragma unroll
;         for (int i = 0; i < 16; ++i) sc[i] = __builtin_amdgcn_exp2f(sc[i]);
; #pragma unroll
;         for (int i = 0; i < 4; ++i) l += (f32x4){sc[4 * i], sc[4 * i + 1], sc[4 * i + 2], sc[4 * i + 3]};
;     };
;     auto pack8 = [&](const f32x16& s0, const f32x16& s1) __attribute__((always_inline)) -> v8i { v8i p;
; #pragma unroll
;         for (int g = 0; g < 4; ++g) { p[g] = (int)pk4_fp8_div16(s0[4 * g], s0[4 * g + 1], s0[4 * g + 2], s0[4 * g + 3]); p[4 + g] = (int)pk4_fp8_div16(s1[4 * g], s1[4 * g + 1], s1[4 * g + 2], s1[4 * g + 3]); }
;         return p; };
;     auto pack4 = [&](const f32x16& sc, v8i& p, const int o) __attribute__((always_inline)) {
; #pragma unroll
;         for (int g = 0; g < 4; ++g) p[o + g] = (int)pk4_fp8_div16(sc[4 * g], sc[4 * g + 1], sc[4 * g + 2], sc[4 * g + 3]); };
;     auto qk = [&](const unsigned char* Kb, int hh, f32x16& sa, f32x16& sb) __attribute__((always_inline)) { const v8i kf = rd32(Kb + koff + hh * 32 * A8_PITCH);
;         sa = mfma8(kf, qfa, (f32x16){}); sb = mfma8(kf, qfb, (f32x16){}); };
;     gload(a.t0, kreg0, vreg0); gload(a.t0 + 1, kreg1, vreg1); lstore(0, kreg0, vreg0); lstore(1, kreg1, vreg1);
;     gload(a.t0 + 2, kreg0, vreg0); lstore(2, kreg0, vreg0);
;     __syncthreads();
;     asm volatile("" : "+v"(qfa), "+v"(qfb));
;     f32x16 s0a, s0b, s1a, s1b;
;     qk(lds, 0, s0a, s0b);
;     if (wid >= 4) __builtin_amdgcn_s_setprio(1);
;     int sb = 0;
;     const v8i zz8 = (v8i){0, 0, 0, 0, 0, 0, 0, 0};
;     v8i PaX = zz8, PbX = zz8, PaY = zz8, PbY = zz8, vX0 = zz8, vX1 = zz8, vY0 = zz8, vY1 = zz8;
;     auto tile = [&](const unsigned char* Kb, const unsigned char* Kn, v8i& Pa, v8i& Pb, v8i& v0, v8i& v1, const v8i& Qa, const v8i& Qb, const v8i& w0, const v8i& w1) __attribute__((always_inline)) {
;         qk(Kb, 1, s1a, s1b);
;         v0 = rd32(Kb + voff); v1 = rd32(Kb + voff + 32 * A8_PITCH);
;         o0[0] = mfma8(w0, Qa, o0[0]); o1[0] = mfma8(w0, Qb, o1[0]); o0[1] = mfma8(w1, Qa, o0[1]); o1[1] = mfma8(w1, Qb, o1[1]);
;         expsum(s0a, l0); expsum(s0b, l1); pack4(s0a, Pa, 0); pack4(s0b, Pb, 0);
;         qk(Kn, 0, s0a, s0b);
;         expsum(s1a, l0); expsum(s1b, l1); pack4(s1a, Pa, 4); pack4(s1b, Pb, 4);
; #pragma unroll
.LBB0_663:
	s_cmp_gt_i32 s16, 3
	s_cselect_b32 s17, -4, 1
	s_add_i32 s18, s17, s16
	s_mul_i32 s6, s16, 0x2800
	s_cmp_gt_i32 s16, 2
	v_mfma_f32_32x32x64_f8f6f4 v[50:65], v[154:161], v[138:145], v[50:65]
	v_exp_f32_e32 v192, v90
	v_add_u32_e32 v90, s6, v218
	s_cselect_b32 s6, -3, 2
	s_add_i32 s6, s6, s16
	s_cmp_gt_i32 s16, 1
	s_cselect_b32 s19, -2, 3
	s_add_i32 s19, s19, s16
	s_cmp_gt_i32 s16, 0
	s_cselect_b32 s49, -1, 4
	s_min_u32 s54, s46, 64
	s_add_i32 s49, s49, s16
	s_cmp_lt_u32 s46, 61
	s_mul_i32 s17, s6, 0x2800
	s_mov_b32 s16, s6
	s_cselect_b64 s[52:53], -1, 0
	s_lshl_b32 s6, s54, 6
	s_add_i32 s54, s6, 0xc0
	s_add_i32 s55, s6, 0xfffff0c0
	s_and_b64 s[52:53], s[52:53], exec
	v_lshl_add_u64 v[98:99], v[182:183], 0, s[6:7]
	s_cselect_b32 s6, s54, s55
	s_cselect_b32 s53, s21, s48
	s_cselect_b32 s52, s20, s47
	s_min_u32 s56, s46, 63
	v_exp_f32_e32 v198, v82
	v_exp_f32_e32 v199, v83
	v_exp_f32_e32 v196, v84
	v_exp_f32_e32 v197, v85
	v_exp_f32_e32 v200, v86
	v_exp_f32_e32 v201, v87
	v_exp_f32_e32 v194, v88
	v_exp_f32_e32 v195, v89
	ds_read_b128 v[82:85], v90 offset:2560
	ds_read_b128 v[86:89], v90 offset:2576
	global_load_dwordx2 v[202:203], v[98:99], off offset:192
	v_add_u32_e32 v98, s6, v215
	s_cmp_lt_u32 s46, 60
	v_ashrrev_i32_e32 v99, 31, v98
	s_cselect_b64 s[54:55], -1, 0
	s_lshl_b32 s6, s56, 6
	v_lshlrev_b64 v[98:99], 8, v[98:99]
	s_add_i32 s56, s6, 0x100
	s_add_i32 s57, s6, 0xfffff100
	v_lshl_add_u64 v[98:99], s[52:53], 0, v[98:99]
	s_and_b64 s[52:53], s[54:55], exec
	s_cselect_b32 s54, s56, s57
	v_lshl_add_u64 v[220:221], v[98:99], 0, v[178:179]
	v_add_u32_e32 v98, s54, v215
	v_ashrrev_i32_e32 v99, 31, v98
	s_cselect_b32 s53, s21, s48
	s_cselect_b32 s52, s20, s47
	v_lshlrev_b64 v[98:99], 8, v[98:99]
	v_lshl_add_u64 v[100:101], v[182:183], 0, s[6:7]
	v_lshl_add_u64 v[98:99], s[52:53], 0, v[98:99]
	global_load_dwordx2 v[204:205], v[100:101], off offset:256
	v_lshl_add_u64 v[222:223], v[98:99], 0, v[178:179]
	s_waitcnt lgkmcnt(0)
	v_mfma_f32_32x32x64_f8f6f4 v[98:113], v[82:89], v[114:121], 0
	v_exp_f32_e32 v193, v91
	v_exp_f32_e32 v224, v92
	v_exp_f32_e32 v225, v93
	v_exp_f32_e32 v226, v94
	v_exp_f32_e32 v227, v95
	v_exp_f32_e32 v228, v96
	v_exp_f32_e32 v229, v97
	ds_read_b128 v[170:173], v90 offset:5120
	ds_read_b128 v[174:177], v90 offset:5136
	ds_read_b128 v[162:165], v90 offset:7680
	ds_read_b128 v[166:169], v90 offset:7696
	v_pk_add_f32 v[90:91], v[186:187], v[198:199]
	v_pk_add_f32 v[92:93], v[184:185], v[196:197]
	v_pk_add_f32 v[90:91], v[200:201], v[90:91]
	v_pk_add_f32 v[92:93], v[194:195], v[92:93]
	v_pk_add_f32 v[90:91], v[192:193], v[90:91]
	v_pk_add_f32 v[92:93], v[224:225], v[92:93]
	v_exp_f32_e32 v66, v66
	v_exp_f32_e32 v67, v67
	v_exp_f32_e32 v68, v68
	v_exp_f32_e32 v69, v69
	v_exp_f32_e32 v70, v70
	v_exp_f32_e32 v71, v71
	v_exp_f32_e32 v72, v72
	v_pk_add_f32 v[230:231], v[228:229], v[92:93]
	v_pk_add_f32 v[232:233], v[226:227], v[90:91]
	v_mfma_f32_32x32x64_f8f6f4 v[82:97], v[82:89], v[122:129], 0
	v_exp_f32_e32 v73, v73
	v_exp_f32_e32 v74, v74
	v_exp_f32_e32 v75, v75
	v_exp_f32_e32 v76, v76
	v_exp_f32_e32 v77, v77
	v_exp_f32_e32 v78, v78
	v_exp_f32_e32 v79, v79
	v_exp_f32_e32 v80, v80
	v_exp_f32_e32 v81, v81
	v_pk_add_f32 v[186:187], v[190:191], v[66:67]
	v_pk_add_f32 v[188:189], v[188:189], v[68:69]
	v_pk_add_f32 v[186:187], v[70:71], v[186:187]
	v_pk_add_f32 v[188:189], v[72:73], v[188:189]
	v_cvt_scalef32_pk_fp8_f32 v184, v198, v199, s36
	v_pk_add_f32 v[186:187], v[74:75], v[186:187]
	v_pk_add_f32 v[188:189], v[76:77], v[188:189]
	v_cvt_scalef32_pk_fp8_f32 v185, v200, v201, s36
	v_cvt_scalef32_pk_fp8_f32 v184, v196, v197, s36 op_sel:[0,0,0,1]
	v_pk_add_f32 v[190:191], v[78:79], v[186:187]
	v_pk_add_f32 v[188:189], v[80:81], v[188:189]
	v_mfma_f32_32x32x64_f8f6f4 v[2:17], v[154:161], v[130:137], v[2:17]
	s_mulk_i32 s18, 0x2800
	v_cvt_scalef32_pk_fp8_f32 v186, v192, v193, s36
	v_cvt_scalef32_pk_fp8_f32 v187, v226, v227, s36
	v_cvt_scalef32_pk_fp8_f32 v154, v66, v67, s36
	v_cvt_scalef32_pk_fp8_f32 v155, v70, v71, s36
	v_cvt_scalef32_pk_fp8_f32 v156, v74, v75, s36
	v_cvt_scalef32_pk_fp8_f32 v157, v78, v79, s36
	v_cvt_scalef32_pk_fp8_f32 v185, v194, v195, s36 op_sel:[0,0,0,1]
	v_add_u32_e32 v219, s18, v218
	v_cvt_scalef32_pk_fp8_f32 v186, v224, v225, s36 op_sel:[0,0,0,1]
	v_cvt_scalef32_pk_fp8_f32 v187, v228, v229, s36 op_sel:[0,0,0,1]
	v_cvt_scalef32_pk_fp8_f32 v154, v68, v69, s36 op_sel:[0,0,0,1]
	v_cvt_scalef32_pk_fp8_f32 v155, v72, v73, s36 op_sel:[0,0,0,1]
	v_cvt_scalef32_pk_fp8_f32 v156, v76, v77, s36 op_sel:[0,0,0,1]
	v_cvt_scalef32_pk_fp8_f32 v157, v80, v81, s36 op_sel:[0,0,0,1]
	v_exp_f32_e32 v98, v98
	v_exp_f32_e32 v99, v99
	v_mfma_f32_32x32x64_f8f6f4 v[34:49], v[146:153], v[138:145], v[34:49]
	v_exp_f32_e32 v100, v100
	v_exp_f32_e32 v101, v101
	v_exp_f32_e32 v102, v102
	v_exp_f32_e32 v103, v103
	v_exp_f32_e32 v104, v104
	v_exp_f32_e32 v105, v105
	v_exp_f32_e32 v106, v106
	v_exp_f32_e32 v107, v107
	v_exp_f32_e32 v108, v108
	v_exp_f32_e32 v109, v109
	v_exp_f32_e32 v110, v110
	v_exp_f32_e32 v111, v111
	v_exp_f32_e32 v112, v112
	v_exp_f32_e32 v113, v113
	ds_read_b128 v[192:195], v219
	ds_read_b128 v[196:199], v219 offset:16
	v_pk_add_f32 v[66:67], v[232:233], v[98:99]
	v_pk_add_f32 v[68:69], v[230:231], v[100:101]
	v_pk_add_f32 v[66:67], v[102:103], v[66:67]
	v_pk_add_f32 v[68:69], v[104:105], v[68:69]
	v_pk_add_f32 v[66:67], v[106:107], v[66:67]
	v_pk_add_f32 v[68:69], v[108:109], v[68:69]
	v_pk_add_f32 v[140:141], v[110:111], v[66:67]
	v_pk_add_f32 v[138:139], v[112:113], v[68:69]
	v_mfma_f32_32x32x64_f8f6f4 v[18:33], v[146:153], v[130:137], v[18:33]
	v_exp_f32_e32 v82, v82
	v_exp_f32_e32 v83, v83
	v_exp_f32_e32 v84, v84
	v_exp_f32_e32 v85, v85
	v_exp_f32_e32 v86, v86
	v_exp_f32_e32 v87, v87
	v_exp_f32_e32 v88, v88
	v_exp_f32_e32 v89, v89
	v_exp_f32_e32 v90, v90
	v_exp_f32_e32 v91, v91
	v_exp_f32_e32 v92, v92
	v_exp_f32_e32 v93, v93
	v_exp_f32_e32 v94, v94
	v_exp_f32_e32 v95, v95
	v_exp_f32_e32 v96, v96
	v_exp_f32_e32 v97, v97
	v_pk_add_f32 v[66:67], v[190:191], v[82:83]
	v_pk_add_f32 v[68:69], v[188:189], v[84:85]
	v_pk_add_f32 v[66:67], v[86:87], v[66:67]
	v_pk_add_f32 v[68:69], v[88:89], v[68:69]
	v_pk_add_f32 v[130:131], v[90:91], v[66:67]
	v_pk_add_f32 v[132:133], v[92:93], v[68:69]
	s_waitcnt lgkmcnt(0)
; DI void attn_unit_d8(unsigned char* lds, const AttnArgs& a) {
;     ...
;     auto expsum = [&](f32x16& sc, f32x4& l) __attribute__((always_inline)) {
; #pragma unroll
;         for (int i = 0; i < 16; ++i) sc[i] = __builtin_amdgcn_exp2f(sc[i]);
; #pragma unroll
;         for (int i = 0; i < 4; ++i) l += (f32x4){sc[4 * i], sc[4 * i + 1], sc[4 * i + 2], sc[4 * i + 3]};
;     };
;     auto pack8 = [&](const f32x16& s0, const f32x16& s1) __attribute__((always_inline)) -> v8i { v8i p;
; #pragma unroll
;         for (int g = 0; g < 4; ++g) { p[g] = (int)pk4_fp8_div16(s0[4 * g], s0[4 * g + 1], s0[4 * g + 2], s0[4 * g + 3]); p[4 + g] = (int)pk4_fp8_div16(s1[4 * g], s1[4 * g + 1], s1[4 * g + 2], s1[4 * g + 3]); }
;         return p; };
;     auto pack4 = [&](const f32x16& sc, v8i& p, const int o) __attribute__((always_inline)) {
; #pragma unroll
;         for (int g = 0; g < 4; ++g) p[o + g] = (int)pk4_fp8_div16(sc[4 * g], sc[4 * g + 1], sc[4 * g + 2], sc[4 * g + 3]); };
;     auto qk = [&](const unsigned char* Kb, int hh, f32x16& sa, f32x16& sb) __attribute__((always_inline)) { const v8i kf = rd32(Kb + koff + hh * 32 * A8_PITCH);
;         sa = mfma8(kf, qfa, (f32x16){}); sb = mfma8(kf, qfb, (f32x16){}); };
;     gload(a.t0, kreg0, vreg0); gload(a.t0 + 1, kreg1, vreg1); lstore(0, kreg0, vreg0); lstore(1, kreg1, vreg1);
;     gload(a.t0 + 2, kreg0, vreg0); lstore(2, kreg0, vreg0);
;     __syncthreads();
;     asm volatile("" : "+v"(qfa), "+v"(qfb));
;     f32x16 s0a, s0b, s1a, s1b;
;     qk(lds, 0, s0a, s0b);
;     if (wid >= 4) __builtin_amdgcn_s_setprio(1);
;     int sb = 0;
;     const v8i zz8 = (v8i){0, 0, 0, 0, 0, 0, 0, 0};
;     v8i PaX = zz8, PbX = zz8, PaY = zz8, PbY = zz8, vX0 = zz8, vX1 = zz8, vY0 = zz8, vY1 = zz8;
;     auto tile = [&](const unsigned char* Kb, const unsigned char* Kn, v8i& Pa, v8i& Pb, v8i& v0, v8i& v1, const v8i& Qa, const v8i& Qb, const v8i& w0, const v8i& w1) __attribute__((always_inline)) {
;         qk(Kb, 1, s1a, s1b);
;         v0 = rd32(Kb + voff); v1 = rd32(Kb + voff + 32 * A8_PITCH);
;         o0[0] = mfma8(w0, Qa, o0[0]); o1[0] = mfma8(w0, Qb, o1[0]); o0[1] = mfma8(w1, Qa, o0[1]); o1[1] = mfma8(w1, Qb, o1[1]);
;         expsum(s0a, l0); expsum(s0b, l1); pack4(s0a, Pa, 0); pack4(s0b, Pb, 0);
;         qk(Kn, 0, s0a, s0b);
;         expsum(s1a, l0); expsum(s1b, l1); pack4(s1a, Pa, 4); pack4(s1b, Pb, 4);
; #pragma unroll
	v_mfma_f32_32x32x64_f8f6f4 v[66:81], v[192:199], v[114:121], 0
	v_cvt_scalef32_pk_fp8_f32 v188, v98, v99, s36
	v_cvt_scalef32_pk_fp8_f32 v189, v102, v103, s36
	v_cvt_scalef32_pk_fp8_f32 v190, v106, v107, s36
	v_cvt_scalef32_pk_fp8_f32 v191, v110, v111, s36
	v_cvt_scalef32_pk_fp8_f32 v158, v82, v83, s36
	v_cvt_scalef32_pk_fp8_f32 v159, v86, v87, s36
	v_pk_add_f32 v[142:143], v[96:97], v[132:133]
	v_pk_add_f32 v[144:145], v[94:95], v[130:131]
	v_cvt_scalef32_pk_fp8_f32 v160, v90, v91, s36
	v_cvt_scalef32_pk_fp8_f32 v188, v100, v101, s36 op_sel:[0,0,0,1]
	v_cvt_scalef32_pk_fp8_f32 v189, v104, v105, s36 op_sel:[0,0,0,1]
	v_cvt_scalef32_pk_fp8_f32 v190, v108, v109, s36 op_sel:[0,0,0,1]
	v_cvt_scalef32_pk_fp8_f32 v191, v112, v113, s36 op_sel:[0,0,0,1]
	v_cvt_scalef32_pk_fp8_f32 v158, v84, v85, s36 op_sel:[0,0,0,1]
	v_cvt_scalef32_pk_fp8_f32 v159, v88, v89, s36 op_sel:[0,0,0,1]
	v_mfma_f32_32x32x64_f8f6f4 v[98:113], v[192:199], v[122:129], 0
	global_load_dwordx2 v[192:193], v[220:221], off
	global_load_dwordx2 v[194:195], v[222:223], off
	ds_read_b128 v[130:133], v219 offset:2560
	ds_read_b128 v[134:137], v219 offset:2576
	s_mulk_i32 s19, 0x2800
	v_exp_f32_e32 v146, v66
	s_add_i32 s80, s61, 0
	v_exp_f32_e32 v147, v67
	s_lshr_b32 s73, s80, 2
	v_exp_f32_e32 v148, v68
	s_lshl_b32 s73, s73, 9
	v_exp_f32_e32 v149, v69
	s_add_i32 s73, s73, s42
	s_add_i32 s19, s19, 0
	v_cvt_scalef32_pk_fp8_f32 v161, v94, v95, s36
	v_exp_f32_e32 v150, v70
	s_mul_i32 s75, s73, 0xaaab
	v_exp_f32_e32 v151, v71
	s_lshr_b32 s75, s75, 22
	v_exp_f32_e32 v152, v72
	s_mul_i32 s76, s75, 0x60
	v_exp_f32_e32 v153, v73
	s_sub_i32 s76, s73, s76
	v_add_u32_e32 v224, s19, v216
	v_add_u32_e32 v225, s19, v217
	v_cvt_scalef32_pk_fp8_f32 v160, v92, v93, s36 op_sel:[0,0,0,1]
	v_cvt_scalef32_pk_fp8_f32 v161, v96, v97, s36 op_sel:[0,0,0,1]
	v_exp_f32_e32 v196, v74
	s_lshr_b32 s77, s76, 6
	v_exp_f32_e32 v197, v75
	s_lshl_b32 s78, s77, 6
	v_exp_f32_e32 v198, v76
	s_sub_i32 s76, s76, s78
	v_exp_f32_e32 v199, v77
	s_sub_i32 s78, 3, s77
	v_exp_f32_e32 v200, v78
	s_lshr_b32 s79, s76, s78
	v_exp_f32_e32 v201, v79
	s_lshl_b32 s79, s79, 2
	v_exp_f32_e32 v220, v80
	s_and_b32 s81, s80, 3
	v_exp_f32_e32 v221, v81
	s_add_i32 s79, s79, s81
	s_waitcnt lgkmcnt(0)
	v_mfma_f32_32x32x64_f8f6f4 v[82:97], v[130:137], v[114:121], 0
	v_add_f32_e64 v66, v140, v146
	v_add_f32_e64 v67, v141, v147
	v_add_f32_e64 v68, v138, v148
	v_add_f32_e64 v69, v139, v149
	v_add_f32_e64 v66, v150, v66
	v_add_f32_e64 v67, v151, v67
	v_add_f32_e64 v68, v152, v68
	v_add_f32_e64 v69, v153, v69
	v_add_f32_e64 v138, v196, v66
	v_add_f32_e64 v139, v197, v67
	v_add_f32_e64 v140, v198, v68
	v_add_f32_e64 v141, v199, v69
	v_exp_f32_e32 v98, v98
	s_lshl_b32 s79, s79, 5
	v_exp_f32_e32 v99, v99
	s_lshl_b32 s81, s63, 2
	v_exp_f32_e32 v100, v100
	s_add_i32 s81, s81, s79
	v_exp_f32_e32 v101, v101
	s_sub_i32 s78, 13, s77
	v_exp_f32_e32 v102, v102
	s_lshl_b32 s81, s81, s78
	v_exp_f32_e32 v103, v103
	s_lshr_b32 s78, 7, s77
	v_exp_f32_e32 v104, v104
	s_and_b32 s78, s76, s78
	v_exp_f32_e32 v105, v105
	s_lshl_b32 s72, s78, 10
	v_exp_f32_e32 v106, v106
	s_add_i32 s81, s81, s72
	v_exp_f32_e32 v107, v107
	s_add_i32 s72, s75, 0
	v_exp_f32_e32 v108, v108
	s_sub_i32 s80, 23, s77
	v_exp_f32_e32 v109, v109
	s_lshl_b32 s72, s72, s80
	v_exp_f32_e32 v110, v110
	s_add_i32 s81, s81, s72
	v_exp_f32_e32 v111, v111
	s_cmp_eq_u32 s77, 0
	s_cselect_b64 s[84:85], s[66:67], s[68:69]
	v_exp_f32_e32 v112, v112
	s_add_u32 s84, s84, s81
	s_addc_u32 s85, s85, 0
	v_exp_f32_e32 v113, v113
	s_lshr_b32 s80, 0x2000, s77
	v_mfma_f32_32x32x64_f8f6f4 v[66:81], v[130:137], v[122:129], 0
	v_add_f32_e64 v130, v144, v98
	v_add_f32_e64 v131, v145, v99
	v_add_f32_e64 v132, v142, v100
	v_add_f32_e64 v133, v143, v101
	v_add_f32_e64 v142, v102, v130
	v_add_f32_e64 v143, v103, v131
	v_add_f32_e64 v132, v104, v132
	v_add_f32_e64 v133, v105, v133
	v_add_f32_e64 v134, v220, v140
	v_add_f32_e64 v135, v221, v141
	v_add_f32_e64 v136, v200, v138
	v_add_f32_e64 v137, v201, v139
	v_pk_add_f32 v[142:143], v[106:107], v[142:143]
	v_pk_add_f32 v[132:133], v[108:109], v[132:133]
	v_cvt_scalef32_pk_fp8_f32 v138, v146, v147, s36
	v_cvt_scalef32_pk_fp8_f32 v139, v150, v151, s36
	v_cvt_scalef32_pk_fp8_f32 v140, v196, v197, s36
	v_cvt_scalef32_pk_fp8_f32 v141, v200, v201, s36
	v_cvt_scalef32_pk_fp8_f32 v130, v98, v99, s36
	v_cvt_scalef32_pk_fp8_f32 v131, v102, v103, s36
	v_pk_add_f32 v[146:147], v[112:113], v[132:133]
	v_pk_add_f32 v[150:151], v[110:111], v[142:143]
	v_mfma_f32_32x32x64_f8f6f4 v[50:65], v[170:177], v[184:191], v[50:65]
	v_exp_f32_e32 v82, v82
	s_and_b32 s72, s78, 3
	v_exp_f32_e32 v83, v83
	s_lshl_b32 s72, s72, 19
	v_exp_f32_e32 v84, v84
	s_lshr_b32 s81, s78, 2
	v_exp_f32_e32 v85, v85
; DI void attn_unit_d8(unsigned char* lds, const AttnArgs& a) {
;     ...
;     auto expsum = [&](f32x16& sc, f32x4& l) __attribute__((always_inline)) {
; #pragma unroll
;         for (int i = 0; i < 16; ++i) sc[i] = __builtin_amdgcn_exp2f(sc[i]);
; #pragma unroll
;         for (int i = 0; i < 4; ++i) l += (f32x4){sc[4 * i], sc[4 * i + 1], sc[4 * i + 2], sc[4 * i + 3]};
;     };
;     auto pack8 = [&](const f32x16& s0, const f32x16& s1) __attribute__((always_inline)) -> v8i { v8i p;
; #pragma unroll
;         for (int g = 0; g < 4; ++g) { p[g] = (int)pk4_fp8_div16(s0[4 * g], s0[4 * g + 1], s0[4 * g + 2], s0[4 * g + 3]); p[4 + g] = (int)pk4_fp8_div16(s1[4 * g], s1[4 * g + 1], s1[4 * g + 2], s1[4 * g + 3]); }
;         return p; };
;     auto pack4 = [&](const f32x16& sc, v8i& p, const int o) __attribute__((always_inline)) {
; #pragma unroll
;         for (int g = 0; g < 4; ++g) p[o + g] = (int)pk4_fp8_div16(sc[4 * g], sc[4 * g + 1], sc[4 * g + 2], sc[4 * g + 3]); };
;     auto qk = [&](const unsigned char* Kb, int hh, f32x16& sa, f32x16& sb) __attribute__((always_inline)) { const v8i kf = rd32(Kb + koff + hh * 32 * A8_PITCH);
;         sa = mfma8(kf, qfa, (f32x16){}); sb = mfma8(kf, qfb, (f32x16){}); };
;     gload(a.t0, kreg0, vreg0); gload(a.t0 + 1, kreg1, vreg1); lstore(0, kreg0, vreg0); lstore(1, kreg1, vreg1);
;     gload(a.t0 + 2, kreg0, vreg0); lstore(2, kreg0, vreg0);
;     __syncthreads();
;     asm volatile("" : "+v"(qfa), "+v"(qfb));
;     f32x16 s0a, s0b, s1a, s1b;
;     qk(lds, 0, s0a, s0b);
;     if (wid >= 4) __builtin_amdgcn_s_setprio(1);
;     int sb = 0;
;     const v8i zz8 = (v8i){0, 0, 0, 0, 0, 0, 0, 0};
;     v8i PaX = zz8, PbX = zz8, PaY = zz8, PbY = zz8, vX0 = zz8, vX1 = zz8, vY0 = zz8, vY1 = zz8;
;     auto tile = [&](const unsigned char* Kb, const unsigned char* Kn, v8i& Pa, v8i& Pb, v8i& v0, v8i& v1, const v8i& Qa, const v8i& Qb, const v8i& w0, const v8i& w1) __attribute__((always_inline)) {
;         qk(Kb, 1, s1a, s1b);
;         v0 = rd32(Kb + voff); v1 = rd32(Kb + voff + 32 * A8_PITCH);
;         o0[0] = mfma8(w0, Qa, o0[0]); o1[0] = mfma8(w0, Qb, o1[0]); o0[1] = mfma8(w1, Qa, o0[1]); o1[1] = mfma8(w1, Qb, o1[1]);
;         expsum(s0a, l0); expsum(s0b, l1); pack4(s0a, Pa, 0); pack4(s0b, Pb, 0);
;         qk(Kn, 0, s0a, s0b);
;         expsum(s1a, l0); expsum(s1b, l1); pack4(s1a, Pa, 4); pack4(s1b, Pb, 4);
; #pragma unroll
	s_lshl_b32 s81, s81, 17
	v_add_u32_e32 v102, s17, v218
	v_exp_f32_e32 v86, v86
	s_add_i32 s72, s72, s81
	v_exp_f32_e32 v87, v87
	s_lshl_b32 s81, s78, 18
	v_exp_f32_e32 v88, v88
	s_cmp_eq_u32 s77, 0
	s_cselect_b32 s72, s72, s81
	v_exp_f32_e32 v89, v89
	s_mul_i32 s81, s77, 0x10000000
	v_cvt_scalef32_pk_fp8_f32 v130, v100, v101, s36 op_sel:[0,0,0,1]
	v_cvt_scalef32_pk_fp8_f32 v131, v104, v105, s36 op_sel:[0,0,0,1]
	v_exp_f32_e32 v90, v90
	s_add_i32 s81, s81, 0x1094000
	v_exp_f32_e32 v91, v91
	s_add_i32 s72, s72, s79
	v_exp_f32_e32 v92, v92
	s_sub_i32 s73, 21, s77
	v_exp_f32_e32 v93, v93
	s_lshl_b32 s73, s75, s73
	ds_read_b128 v[98:101], v102
	ds_read_b128 v[102:105], v102 offset:16
	v_cvt_scalef32_pk_fp8_f32 v138, v148, v149, s36 op_sel:[0,0,0,1]
	v_cvt_scalef32_pk_fp8_f32 v139, v152, v153, s36 op_sel:[0,0,0,1]
	v_cvt_scalef32_pk_fp8_f32 v140, v198, v199, s36 op_sel:[0,0,0,1]
	v_cvt_scalef32_pk_fp8_f32 v141, v220, v221, s36 op_sel:[0,0,0,1]
	v_exp_f32_e32 v94, v94
	s_add_i32 s72, s72, s73
	v_mfma_f32_32x32x64_f8f6f4 v[2:17], v[170:177], v[154:161], v[2:17]
	v_exp_f32_e32 v148, v96
	s_add_u32 s72, s72, s81
	v_cvt_scalef32_pk_fp8_f32 v132, v106, v107, s36
	v_exp_f32_e32 v149, v97
	s_or_b32 s79, s72, s77
	v_pk_add_f32 v[96:97], v[136:137], v[82:83]
	v_pk_add_f32 v[106:107], v[134:135], v[84:85]
	v_exp_f32_e32 v66, v66
	v_exp_f32_e32 v67, v67
	v_exp_f32_e32 v68, v68
	v_exp_f32_e32 v69, v69
	v_exp_f32_e32 v95, v95
	v_cvt_scalef32_pk_fp8_f32 v133, v110, v111, s36
	v_pk_add_f32 v[106:107], v[88:89], v[106:107]
	v_pk_add_f32 v[96:97], v[86:87], v[96:97]
	v_exp_f32_e32 v70, v70
	v_exp_f32_e32 v71, v71
	v_exp_f32_e32 v72, v72
	v_exp_f32_e32 v73, v73
	v_cvt_scalef32_pk_fp8_f32 v132, v108, v109, s36 op_sel:[0,0,0,1]
	v_cvt_scalef32_pk_fp8_f32 v133, v112, v113, s36 op_sel:[0,0,0,1]
	v_pk_add_f32 v[96:97], v[90:91], v[96:97]
	v_pk_add_f32 v[106:107], v[92:93], v[106:107]
	v_exp_f32_e32 v74, v74
	v_mfma_f32_32x32x64_f8f6f4 v[34:49], v[162:169], v[184:191], v[34:49]
	v_exp_f32_e32 v75, v75
	v_exp_f32_e32 v76, v76
	v_exp_f32_e32 v77, v77
	v_exp_f32_e32 v78, v78
	v_exp_f32_e32 v79, v79
	v_exp_f32_e32 v80, v80
	v_exp_f32_e32 v81, v81
	v_cvt_scalef32_pk_fp8_f32 v142, v82, v83, s36
	v_cvt_scalef32_pk_fp8_f32 v143, v86, v87, s36
	v_cvt_scalef32_pk_fp8_f32 v144, v90, v91, s36
	v_cvt_scalef32_pk_fp8_f32 v142, v84, v85, s36 op_sel:[0,0,0,1]
	v_pk_add_f32 v[82:83], v[150:151], v[66:67]
	v_pk_add_f32 v[84:85], v[146:147], v[68:69]
	s_mulk_i32 s49, 0x2800
	v_pk_add_f32 v[184:185], v[148:149], v[106:107]
	v_pk_add_f32 v[186:187], v[94:95], v[96:97]
	v_cvt_scalef32_pk_fp8_f32 v145, v94, v95, s36
	v_cvt_scalef32_pk_fp8_f32 v143, v88, v89, s36 op_sel:[0,0,0,1]
	v_cvt_scalef32_pk_fp8_f32 v144, v92, v93, s36 op_sel:[0,0,0,1]
	v_mfma_f32_32x32x64_f8f6f4 v[18:33], v[162:169], v[154:161], v[18:33]
	v_add_f32_e64 v84, v72, v84
	v_add_f32_e64 v85, v73, v85
	v_add_f32_e64 v82, v70, v82
	v_add_f32_e64 v83, v71, v83
	s_add_i32 s6, s49, 0
	v_add_f32_e64 v82, v74, v82
	v_add_f32_e64 v83, v75, v83
	v_add_f32_e64 v84, v76, v84
	v_add_f32_e64 v85, v77, v85
	v_cvt_scalef32_pk_fp8_f32 v134, v66, v67, s36
	v_cvt_scalef32_pk_fp8_f32 v135, v70, v71, s36
	v_cvt_scalef32_pk_fp8_f32 v136, v74, v75, s36
	v_cvt_scalef32_pk_fp8_f32 v137, v78, v79, s36
	v_pk_add_f32 v[188:189], v[80:81], v[84:85]
	v_pk_add_f32 v[190:191], v[78:79], v[82:83]
	v_add_u32_e32 v106, s6, v216
	v_add_u32_e32 v107, s6, v217
	v_cvt_scalef32_pk_fp8_f32 v145, v148, v149, s36 op_sel:[0,0,0,1]
	v_cvt_scalef32_pk_fp8_f32 v134, v68, v69, s36 op_sel:[0,0,0,1]
	v_cvt_scalef32_pk_fp8_f32 v135, v72, v73, s36 op_sel:[0,0,0,1]
	v_cvt_scalef32_pk_fp8_f32 v136, v76, v77, s36 op_sel:[0,0,0,1]
	v_cvt_scalef32_pk_fp8_f32 v137, v80, v81, s36 op_sel:[0,0,0,1]
	s_waitcnt lgkmcnt(0)
	v_mfma_f32_32x32x64_f8f6f4 v[82:97], v[98:105], v[114:121], 0
	ds_read_b128 v[154:157], v219 offset:5120
	ds_read_b128 v[158:161], v219 offset:5136
	ds_read_b128 v[146:149], v219 offset:7680
	ds_read_b128 v[150:153], v219 offset:7696
	s_cmpk_gt_i32 s42, 0x1ff
	s_cbranch_scc1 .Lmy_rd0_ldum
	s_add_i32 s72, s61, -1
	s_cmp_lt_u32 s72, 24
	s_cbranch_scc0 .Lmy_rd0_noc
	s_waitcnt vmcnt(4)
	v_cvt_scalef32_pk_fp8_f32 v236, v236, v240, s62
	v_cvt_scalef32_pk_fp8_f32 v237, v237, v241, s62
	v_cvt_scalef32_pk_fp8_f32 v238, v238, v242, s62
	v_cvt_scalef32_pk_fp8_f32 v239, v239, v243, s62
	v_cvt_scalef32_pk_fp8_f32 v236, v244, v248, s62 op_sel:[0,0,0,1]
	v_cvt_scalef32_pk_fp8_f32 v237, v245, v249, s62 op_sel:[0,0,0,1]
	v_cvt_scalef32_pk_fp8_f32 v238, v246, v250, s62 op_sel:[0,0,0,1]
	v_cvt_scalef32_pk_fp8_f32 v239, v247, v251, s62 op_sel:[0,0,0,1]
	ds_write_b32 v252, v236
	ds_write_b32 v252, v237 offset:36
	ds_write_b32 v252, v238 offset:72
	ds_write_b32 v252, v239 offset:108

; DI void attn_unit_a8(unsigned char* lds, const AttnArgs& a) {
;     ...
;     auto expsum = [&](f32x16& sc) __attribute__((always_inline)) {
; #pragma unroll
;         for (int i = 0; i < 16; ++i) sc[i] = __builtin_amdgcn_exp2f(sc[i]);
; #pragma unroll
;         for (int i = 0; i < 4; ++i) l0 += (f32x4){sc[4 * i], sc[4 * i + 1], sc[4 * i + 2], sc[4 * i + 3]};
;     };
;     auto pack8 = [&](const f32x16& s0, const f32x16& s1) __attribute__((always_inline)) -> v8i { v8i p;
; #pragma unroll
;         for (int g = 0; g < 4; ++g) { p[g] = (int)pk4_fp8_div16(s0[4 * g], s0[4 * g + 1], s0[4 * g + 2], s0[4 * g + 3]); p[4 + g] = (int)pk4_fp8_div16(s1[4 * g], s1[4 * g + 1], s1[4 * g + 2], s1[4 * g + 3]); }
;         return p; };
;     f32x4 wq[4];
;     const int wn4 = (tid & 63) * 4;
;     constexpr int WPITCH = 36;
;     auto w_decode = [&](int j, const float*& src, unsigned char*& dst, int& ld, int& n0, int& k0, bool& gu) __attribute__((always_inline)) {
;         const int g = (j >> 2) * 512 + a.wl, e = g / 96, rr = g - e * 96; KParamsPtr kp = kparams();
;         if (rr < 64) { src = kp->w_gu + ((size_t)a.wli * NE + e) * (1024 * 2048); dst = kp->ws + WS_WGU + (size_t)a.wli * SZ_WGU + (size_t)e * 2048 * 1024; ld = 2048; n0 = (rr & 7) * 256; k0 = ((rr >> 3) * 4 + (j & 3)) * 32; gu = true; }
;         else { const int q = rr - 64; src = kp->w_dn + ((size_t)a.wli * NE + e) * (1024 * 1024); dst = kp->ws + WS_WDN + (size_t)a.wli * SZ_WDN + (size_t)e * 1024 * 1024; ld = 1024; n0 = (q & 3) * 256; k0 = ((q >> 2) * 4 + (j & 3)) * 32; gu = false; } };
;     auto w_issue = [&](int j) __attribute__((always_inline)) { const float* src; unsigned char* dst; int ld, n0, k0; bool gu; w_decode(j, src, dst, ld, n0, k0, gu);
;         const float* p = src + (size_t)(k0 + 4 * wid) * ld + n0 + wn4;
;         wq[0] = __builtin_nontemporal_load((const f32x4*)p); wq[1] = __builtin_nontemporal_load((const f32x4*)(p + ld));
;         wq[2] = __builtin_nontemporal_load((const f32x4*)(p + (size_t)2 * ld)); wq[3] = __builtin_nontemporal_load((const f32x4*)(p + (size_t)3 * ld)); };
;     auto w_cvt = [&]() __attribute__((always_inline)) { unsigned char* t8 = lds + AT_WT + wn4 * WPITCH + 4 * wid;
; #pragma unroll
;         for (int j = 0; j < 4; ++j) *(unsigned*)(t8 + j * WPITCH) = pk4_fp8_mul64(wq[0][j], wq[1][j], wq[2][j], wq[3][j]); };
;     const int wcol = tid >> 1, whalf = tid & 1;
.LBB0_714:
	s_min_i32 s4, s56, 64
	s_add_i32 s6, s4, 3
	s_cmp_lt_u32 s56, 61
	s_cselect_b64 s[10:11], -1, 0
	s_lshl_b32 s4, s6, 6
	s_add_i32 s7, s4, 0xfffff000
	s_and_b64 s[12:13], s[10:11], exec
	s_cselect_b32 s4, s4, s7
	v_add_u32_e32 v42, s4, v154
	s_add_i32 s4, s8, 1
	s_cmp_lg_u32 s8, 2
	s_mov_b32 s9, s8
	s_cselect_b32 s8, s4, 0
	s_mul_i32 s4, s8, 0x4680
	v_add_u32_e32 v106, s4, v157
	ds_read_b128 v[34:37], v106
	ds_read_b128 v[38:41], v106 offset:16
	s_and_b64 s[10:11], s[10:11], exec
	v_ashrrev_i32_e32 v43, 31, v42
	s_cselect_b32 s10, s58, s60
	s_cselect_b32 s11, s59, s61
	s_ashr_i32 s7, s6, 31
	s_waitcnt lgkmcnt(0)
	v_mfma_f32_32x32x64_f8f6f4 v[50:65], v[34:41], v[98:105], 0
	v_lshlrev_b64 v[34:35], 7, v[42:43]
	s_lshl_b64 s[12:13], s[6:7], 6
	v_lshl_add_u64 v[34:35], s[10:11], 0, v[34:35]
	v_lshl_add_u64 v[34:35], v[34:35], 0, v[130:131]
	v_lshl_add_u64 v[42:43], v[132:133], 0, s[12:13]
	global_load_dwordx2 v[112:113], v[34:35], off
	ds_read_b128 v[34:37], v106 offset:2560
	ds_read_b128 v[38:41], v106 offset:2576
	global_load_dwordx2 v[114:115], v[42:43], off
	s_mulk_i32 s9, 0x4680
	v_add_u32_e32 v42, s9, v157
	v_exp_f32_e32 v82, v82
	v_exp_f32_e32 v83, v83
	v_exp_f32_e32 v86, v86
	v_exp_f32_e32 v87, v87
	v_exp_f32_e32 v90, v90
	v_exp_f32_e32 v91, v91
	v_exp_f32_e32 v94, v94
	v_exp_f32_e32 v95, v95
	v_exp_f32_e32 v124, v66
	v_exp_f32_e32 v125, v67
	v_exp_f32_e32 v146, v70
	v_exp_f32_e32 v147, v71
	v_exp_f32_e32 v74, v74
	v_exp_f32_e32 v75, v75
	v_exp_f32_e32 v78, v78
	v_exp_f32_e32 v79, v79
	ds_read_b128 v[116:119], v42 offset:5120
	ds_read_b128 v[120:123], v42 offset:5136
	ds_read_b128 v[138:141], v42 offset:7680
	ds_read_b128 v[142:145], v42 offset:7696
	v_exp_f32_e32 v84, v84
	v_exp_f32_e32 v85, v85
	v_exp_f32_e32 v88, v88
	v_exp_f32_e32 v89, v89
	v_exp_f32_e32 v92, v92
	v_exp_f32_e32 v93, v93
	v_exp_f32_e32 v96, v96
	v_exp_f32_e32 v97, v97
	v_exp_f32_e32 v126, v68
	v_exp_f32_e32 v127, v69
	v_exp_f32_e32 v148, v72
	v_exp_f32_e32 v149, v73
	v_exp_f32_e32 v76, v76
	v_exp_f32_e32 v77, v77
	v_exp_f32_e32 v80, v80
	v_exp_f32_e32 v81, v81
	v_cvt_scalef32_pk_fp8_f32 v66, v82, v83, s48
	v_cvt_scalef32_pk_fp8_f32 v70, v124, v125, s48
	v_cvt_scalef32_pk_fp8_f32 v67, v86, v87, s48
	v_cvt_scalef32_pk_fp8_f32 v71, v146, v147, s48
	v_cvt_scalef32_pk_fp8_f32 v68, v90, v91, s48
	v_cvt_scalef32_pk_fp8_f32 v72, v74, v75, s48
	v_cvt_scalef32_pk_fp8_f32 v69, v94, v95, s48
	v_cvt_scalef32_pk_fp8_f32 v73, v78, v79, s48
	v_cvt_scalef32_pk_fp8_f32 v66, v84, v85, s48 op_sel:[0,0,0,1]
	v_cvt_scalef32_pk_fp8_f32 v70, v126, v127, s48 op_sel:[0,0,0,1]
	v_cvt_scalef32_pk_fp8_f32 v67, v88, v89, s48 op_sel:[0,0,0,1]
	v_cvt_scalef32_pk_fp8_f32 v71, v148, v149, s48 op_sel:[0,0,0,1]
	v_cvt_scalef32_pk_fp8_f32 v68, v92, v93, s48 op_sel:[0,0,0,1]
	v_cvt_scalef32_pk_fp8_f32 v72, v76, v77, s48 op_sel:[0,0,0,1]
	v_cvt_scalef32_pk_fp8_f32 v69, v96, v97, s48 op_sel:[0,0,0,1]
	v_cvt_scalef32_pk_fp8_f32 v73, v80, v81, s48 op_sel:[0,0,0,1]
	s_waitcnt lgkmcnt(4)
	v_mfma_f32_32x32x64_f8f6f4 v[34:49], v[34:41], v[98:105], 0
	s_addk_i32 s4, 0x4680
	s_cmp_eq_u32 s8, 2
	v_add_f32_e64 v110, v110, v84
	v_add_f32_e64 v111, v111, v85
	v_add_f32_e64 v82, v108, v82
	v_add_f32_e64 v83, v109, v83
	s_cselect_b64 s[6:7], -1, 0
	v_add_f32_e64 v84, v88, v110
	v_add_f32_e64 v85, v89, v111
	v_add_f32_e64 v82, v86, v82
	v_add_f32_e64 v83, v87, v83
	v_add_f32_e64 v84, v92, v84
	v_add_f32_e64 v85, v93, v85
	v_pk_add_f32 v[82:83], v[90:91], v[82:83]
	s_and_b64 s[10:11], s[6:7], exec
	v_pk_add_f32 v[84:85], v[96:97], v[84:85]
	v_pk_add_f32 v[82:83], v[94:95], v[82:83]
	s_cselect_b32 s4, 0, s4
	v_pk_add_f32 v[82:83], v[124:125], v[82:83]
	v_pk_add_f32 v[84:85], v[126:127], v[84:85]
	s_waitcnt lgkmcnt(2)
	v_mfma_f32_32x32x64_f8f6f4 v[18:33], v[116:123], v[66:73], v[18:33]
	s_add_i32 s4, s4, 0
	v_add_f32_e64 v84, v148, v84
	v_add_f32_e64 v85, v149, v85
	v_add_f32_e64 v82, v146, v82
	v_add_f32_e64 v83, v147, v83
	v_add_f32_e64 v76, v76, v84
	v_add_f32_e64 v77, v77, v85
	v_add_f32_e64 v74, v74, v82
	v_add_f32_e64 v75, v75, v83
	v_add_f32_e64 v110, v80, v76
	v_add_f32_e64 v111, v81, v77
	v_add_f32_e64 v108, v78, v74
	v_add_f32_e64 v109, v79, v75
	s_cmpk_gt_u32 s56, 0x42
	s_waitcnt lgkmcnt(0)
	v_mfma_f32_32x32x64_f8f6f4 v[2:17], v[138:145], v[66:73], v[2:17]
	v_add_u32_e32 v66, s4, v155
	s_waitcnt vmcnt(3)
	ds_write_b64 v66, v[134:135]
	v_add_u32_e32 v66, s4, v156
	v_add_u32_e32 v66, 0x1400, v66
	s_waitcnt vmcnt(2)
	ds_write2_b32 v66, v136, v137 offset1:8
	s_waitcnt lgkmcnt(0)
	s_barrier
; DI void attn_unit_a8(unsigned char* lds, const AttnArgs& a) {
;     ...
;     auto expsum = [&](f32x16& sc) __attribute__((always_inline)) {
; #pragma unroll
;         for (int i = 0; i < 16; ++i) sc[i] = __builtin_amdgcn_exp2f(sc[i]);
; #pragma unroll
;         for (int i = 0; i < 4; ++i) l0 += (f32x4){sc[4 * i], sc[4 * i + 1], sc[4 * i + 2], sc[4 * i + 3]};
;     };
;     auto pack8 = [&](const f32x16& s0, const f32x16& s1) __attribute__((always_inline)) -> v8i { v8i p;
; #pragma unroll
;         for (int g = 0; g < 4; ++g) { p[g] = (int)pk4_fp8_div16(s0[4 * g], s0[4 * g + 1], s0[4 * g + 2], s0[4 * g + 3]); p[4 + g] = (int)pk4_fp8_div16(s1[4 * g], s1[4 * g + 1], s1[4 * g + 2], s1[4 * g + 3]); }
;         return p; };
;     f32x4 wq[4];
;     const int wn4 = (tid & 63) * 4;
;     constexpr int WPITCH = 36;
;     auto w_decode = [&](int j, const float*& src, unsigned char*& dst, int& ld, int& n0, int& k0, bool& gu) __attribute__((always_inline)) {
;         const int g = (j >> 2) * 512 + a.wl, e = g / 96, rr = g - e * 96; KParamsPtr kp = kparams();
;         if (rr < 64) { src = kp->w_gu + ((size_t)a.wli * NE + e) * (1024 * 2048); dst = kp->ws + WS_WGU + (size_t)a.wli * SZ_WGU + (size_t)e * 2048 * 1024; ld = 2048; n0 = (rr & 7) * 256; k0 = ((rr >> 3) * 4 + (j & 3)) * 32; gu = true; }
;         else { const int q = rr - 64; src = kp->w_dn + ((size_t)a.wli * NE + e) * (1024 * 1024); dst = kp->ws + WS_WDN + (size_t)a.wli * SZ_WDN + (size_t)e * 1024 * 1024; ld = 1024; n0 = (q & 3) * 256; k0 = ((q >> 2) * 4 + (j & 3)) * 32; gu = false; } };
;     auto w_issue = [&](int j) __attribute__((always_inline)) { const float* src; unsigned char* dst; int ld, n0, k0; bool gu; w_decode(j, src, dst, ld, n0, k0, gu);
;         const float* p = src + (size_t)(k0 + 4 * wid) * ld + n0 + wn4;
;         wq[0] = __builtin_nontemporal_load((const f32x4*)p); wq[1] = __builtin_nontemporal_load((const f32x4*)(p + ld));
;         wq[2] = __builtin_nontemporal_load((const f32x4*)(p + (size_t)2 * ld)); wq[3] = __builtin_nontemporal_load((const f32x4*)(p + (size_t)3 * ld)); };
;     auto w_cvt = [&]() __attribute__((always_inline)) { unsigned char* t8 = lds + AT_WT + wn4 * WPITCH + 4 * wid;
; #pragma unroll
;         for (int j = 0; j < 4; ++j) *(unsigned*)(t8 + j * WPITCH) = pk4_fp8_mul64(wq[0][j], wq[1][j], wq[2][j], wq[3][j]); };
;     const int wcol = tid >> 1, whalf = tid & 1;
	s_cbranch_scc1 .LBB0_716
	s_min_u32 s4, s56, 63
	s_cmp_lt_u32 s56, 60
	s_cselect_b64 s[10:11], -1, 0
	s_lshl_b32 s4, s4, 6
	s_add_i32 s9, s4, 0x100
	s_add_i32 s14, s4, 0xfffff100
	s_and_b64 s[12:13], s[10:11], exec
	s_cselect_b32 s9, s9, s14
	s_add_i32 s8, s8, 1
	s_and_b64 s[6:7], s[6:7], exec
	v_add_u32_e32 v82, s9, v154
	s_cselect_b32 s8, 0, s8
	s_and_b64 s[10:11], s[10:11], exec
	v_ashrrev_i32_e32 v83, 31, v82
	s_cselect_b32 s11, s59, s61
	s_cselect_b32 s10, s58, s60
	v_lshlrev_b64 v[82:83], 7, v[82:83]
	s_mul_i32 s6, s8, 0x4680
	v_lshl_add_u64 v[90:91], s[10:11], 0, v[82:83]
	v_add_u32_e32 v86, s6, v157
	v_lshl_add_u64 v[90:91], v[90:91], 0, v[130:131]
	ds_read_b128 v[66:69], v86 offset:2560
	ds_read_b128 v[70:73], v86 offset:2576
	ds_read_b128 v[82:85], v86
	ds_read_b128 v[86:89], v86 offset:16
	global_load_dwordx2 v[134:135], v[90:91], off
	v_lshl_add_u64 v[90:91], v[132:133], 0, s[4:5]
	global_load_dwordx2 v[136:137], v[90:91], off offset:256
	v_exp_f32_e32 v50, v50
	v_exp_f32_e32 v51, v51
	v_exp_f32_e32 v54, v54
	v_exp_f32_e32 v55, v55
	v_exp_f32_e32 v58, v58
	v_exp_f32_e32 v59, v59
	v_exp_f32_e32 v62, v62
	v_exp_f32_e32 v63, v63
	v_exp_f32_e32 v124, v34
	v_exp_f32_e32 v125, v35
	v_exp_f32_e32 v146, v38
	v_exp_f32_e32 v147, v39
	v_exp_f32_e32 v42, v42
	v_exp_f32_e32 v43, v43
	v_exp_f32_e32 v46, v46
	v_exp_f32_e32 v47, v47
	ds_read_b128 v[116:119], v106 offset:5120
	ds_read_b128 v[120:123], v106 offset:5136
	ds_read_b128 v[138:141], v106 offset:7680
	ds_read_b128 v[142:145], v106 offset:7696
	v_exp_f32_e32 v52, v52
	v_exp_f32_e32 v53, v53
	v_exp_f32_e32 v56, v56
	v_exp_f32_e32 v57, v57
	v_exp_f32_e32 v60, v60
	v_exp_f32_e32 v61, v61
	v_exp_f32_e32 v64, v64
	v_exp_f32_e32 v65, v65
	v_exp_f32_e32 v126, v36
	v_exp_f32_e32 v127, v37
	v_exp_f32_e32 v148, v40
	v_exp_f32_e32 v149, v41
	v_exp_f32_e32 v44, v44
	v_exp_f32_e32 v45, v45
	v_exp_f32_e32 v48, v48
	v_exp_f32_e32 v49, v49
	s_waitcnt lgkmcnt(6)
	v_mfma_f32_32x32x64_f8f6f4 v[66:81], v[66:73], v[98:105], 0
	v_cvt_scalef32_pk_fp8_f32 v34, v50, v51, s48
	v_cvt_scalef32_pk_fp8_f32 v38, v124, v125, s48
	v_cvt_scalef32_pk_fp8_f32 v35, v54, v55, s48
	v_cvt_scalef32_pk_fp8_f32 v39, v146, v147, s48
	v_cvt_scalef32_pk_fp8_f32 v36, v58, v59, s48
	v_cvt_scalef32_pk_fp8_f32 v40, v42, v43, s48
	v_cvt_scalef32_pk_fp8_f32 v37, v62, v63, s48
	v_cvt_scalef32_pk_fp8_f32 v41, v46, v47, s48
	v_cvt_scalef32_pk_fp8_f32 v34, v52, v53, s48 op_sel:[0,0,0,1]
	v_cvt_scalef32_pk_fp8_f32 v38, v126, v127, s48 op_sel:[0,0,0,1]
	v_cvt_scalef32_pk_fp8_f32 v35, v56, v57, s48 op_sel:[0,0,0,1]
	v_cvt_scalef32_pk_fp8_f32 v39, v148, v149, s48 op_sel:[0,0,0,1]
	v_cvt_scalef32_pk_fp8_f32 v36, v60, v61, s48 op_sel:[0,0,0,1]
	v_cvt_scalef32_pk_fp8_f32 v40, v44, v45, s48 op_sel:[0,0,0,1]
	v_cvt_scalef32_pk_fp8_f32 v37, v64, v65, s48 op_sel:[0,0,0,1]
	s_waitcnt lgkmcnt(4)
	v_mfma_f32_32x32x64_f8f6f4 v[82:97], v[82:89], v[98:105], 0
	v_cvt_scalef32_pk_fp8_f32 v41, v48, v49, s48 op_sel:[0,0,0,1]
	v_add_f32_e64 v110, v110, v52
	v_add_f32_e64 v111, v111, v53
	v_add_f32_e64 v50, v108, v50
	v_add_f32_e64 v51, v109, v51
	s_addk_i32 s6, 0x4680
	v_add_f32_e64 v52, v56, v110
	v_add_f32_e64 v53, v57, v111
	v_add_f32_e64 v50, v54, v50
	v_add_f32_e64 v51, v55, v51
	s_cmp_lg_u32 s8, 2
	v_add_f32_e64 v50, v58, v50
	v_add_f32_e64 v51, v59, v51
	v_pk_add_f32 v[52:53], v[60:61], v[52:53]
	s_cselect_b32 s4, s6, 0
	v_pk_add_f32 v[52:53], v[64:65], v[52:53]
	v_pk_add_f32 v[50:51], v[62:63], v[50:51]
	s_add_i32 s4, s4, 0
	v_pk_add_f32 v[50:51], v[124:125], v[50:51]
	v_pk_add_f32 v[52:53], v[126:127], v[52:53]
	s_waitcnt lgkmcnt(2)
	v_mfma_f32_32x32x64_f8f6f4 v[18:33], v[116:123], v[34:41], v[18:33]
	v_add_f32_e64 v52, v148, v52
	v_add_f32_e64 v53, v149, v53
	v_add_f32_e64 v50, v146, v50
	v_add_f32_e64 v51, v147, v51
	v_add_f32_e64 v44, v44, v52
	v_add_f32_e64 v45, v45, v53
	v_add_f32_e64 v42, v42, v50
	v_add_f32_e64 v43, v43, v51
	v_add_f32_e64 v110, v48, v44
	v_add_f32_e64 v111, v49, v45
	v_add_f32_e64 v108, v46, v42
	v_add_f32_e64 v109, v47, v43
	s_waitcnt lgkmcnt(0)
	v_mfma_f32_32x32x64_f8f6f4 v[2:17], v[138:145], v[34:41], v[2:17]
	v_add_u32_e32 v34, s4, v155
	s_waitcnt vmcnt(3)
	ds_write_b64 v34, v[112:113]
	v_add_u32_e32 v34, s4, v156
	v_add_u32_e32 v34, 0x1400, v34
	s_waitcnt vmcnt(2)
	ds_write2_b32 v34, v114, v115 offset1:8
	s_waitcnt lgkmcnt(0)
	s_barrier

; DI void attn_unit_d8(unsigned char* lds, const AttnArgs& a) {
;     ...
;     auto expsum = [&](f32x16& sc, f32x4& l) __attribute__((always_inline)) {
; #pragma unroll
;         for (int i = 0; i < 16; ++i) sc[i] = __builtin_amdgcn_exp2f(sc[i]);
; #pragma unroll
;         for (int i = 0; i < 4; ++i) l += (f32x4){sc[4 * i], sc[4 * i + 1], sc[4 * i + 2], sc[4 * i + 3]};
;     };
;     auto pack8 = [&](const f32x16& s0, const f32x16& s1) __attribute__((always_inline)) -> v8i { v8i p;
; #pragma unroll
;         for (int g = 0; g < 4; ++g) { p[g] = (int)pk4_fp8_div16(s0[4 * g], s0[4 * g + 1], s0[4 * g + 2], s0[4 * g + 3]); p[4 + g] = (int)pk4_fp8_div16(s1[4 * g], s1[4 * g + 1], s1[4 * g + 2], s1[4 * g + 3]); }
;         return p; };
;     auto pack4 = [&](const f32x16& sc, v8i& p, const int o) __attribute__((always_inline)) {
; #pragma unroll
;         for (int g = 0; g < 4; ++g) p[o + g] = (int)pk4_fp8_div16(sc[4 * g], sc[4 * g + 1], sc[4 * g + 2], sc[4 * g + 3]); };
;     auto qk = [&](const unsigned char* Kb, int hh, f32x16& sa, f32x16& sb) __attribute__((always_inline)) { const v8i kf = rd32(Kb + koff + hh * 32 * A8_PITCH);
;         sa = mfma8(kf, qfa, (f32x16){}); sb = mfma8(kf, qfb, (f32x16){}); };
;     gload(a.t0, kreg0, vreg0); gload(a.t0 + 1, kreg1, vreg1); lstore(0, kreg0, vreg0); lstore(1, kreg1, vreg1);
;     gload(a.t0 + 2, kreg0, vreg0); lstore(2, kreg0, vreg0);
;     __syncthreads();
;     asm volatile("" : "+v"(qfa), "+v"(qfb));
;     f32x16 s0a, s0b, s1a, s1b;
;     qk(lds, 0, s0a, s0b);
;     if (wid >= 4) __builtin_amdgcn_s_setprio(1);
;     int sb = 0;
;     const v8i zz8 = (v8i){0, 0, 0, 0, 0, 0, 0, 0};
;     v8i PaX = zz8, PbX = zz8, PaY = zz8, PbY = zz8, vX0 = zz8, vX1 = zz8, vY0 = zz8, vY1 = zz8;
;     auto tile = [&](const unsigned char* Kb, const unsigned char* Kn, v8i& Pa, v8i& Pb, v8i& v0, v8i& v1, const v8i& Qa, const v8i& Qb, const v8i& w0, const v8i& w1) __attribute__((always_inline)) {
;         qk(Kb, 1, s1a, s1b);
;         v0 = rd32(Kb + voff); v1 = rd32(Kb + voff + 32 * A8_PITCH);
;         o0[0] = mfma8(w0, Qa, o0[0]); o1[0] = mfma8(w0, Qb, o1[0]); o0[1] = mfma8(w1, Qa, o0[1]); o1[1] = mfma8(w1, Qb, o1[1]);
;         expsum(s0a, l0); expsum(s0b, l1); pack4(s0a, Pa, 0); pack4(s0b, Pb, 0);
;         qk(Kn, 0, s0a, s0b);
;         expsum(s1a, l0); expsum(s1b, l1); pack4(s1a, Pa, 4); pack4(s1b, Pb, 4);
; #pragma unroll
.LBB0_1888:
	s_add_i32 s22, s22, 2
	s_mul_i32 s8, s23, 0x2800
	s_cmp_gt_i32 s23, 3
	v_mfma_f32_32x32x64_f8f6f4 v[50:65], v[154:161], v[138:145], v[50:65]
	v_exp_f32_e32 v194, v90
	v_add_u32_e32 v90, s8, v219
	s_cselect_b32 s8, -4, 1
	s_add_i32 s51, s8, s23
	s_cmp_gt_i32 s23, 2
	s_cselect_b32 s8, -3, 2
	s_add_i32 s8, s8, s23
	s_cmp_gt_i32 s23, 1
	s_cselect_b32 s52, -2, 3
	s_add_i32 s52, s52, s23
	s_cmp_gt_i32 s23, 0
	s_cselect_b32 s53, -1, 4
	s_min_u32 s56, s22, 64
	s_add_i32 s53, s53, s23
	s_cmp_lt_u32 s22, 61
	s_mul_i32 s50, s8, 0x2800
	s_mov_b32 s23, s8
	s_cselect_b64 s[54:55], -1, 0
	s_lshl_b32 s8, s56, 6
	s_add_i32 s56, s8, 0xc0
	s_add_i32 s57, s8, 0xfffff0c0
	s_and_b64 s[54:55], s[54:55], exec
	v_lshl_add_u64 v[98:99], v[184:185], 0, s[8:9]
	s_cselect_b32 s8, s56, s57
	s_cselect_b32 s55, s19, s21
	s_cselect_b32 s54, s18, s20
	s_min_u32 s58, s22, 63
	v_exp_f32_e32 v200, v82
	v_exp_f32_e32 v201, v83
	v_exp_f32_e32 v198, v84
	v_exp_f32_e32 v199, v85
	v_exp_f32_e32 v202, v86
	v_exp_f32_e32 v203, v87
	v_exp_f32_e32 v196, v88
	v_exp_f32_e32 v197, v89
	ds_read_b128 v[82:85], v90 offset:2560
	ds_read_b128 v[86:89], v90 offset:2576
	global_load_dwordx2 v[204:205], v[98:99], off offset:192
	v_add_u32_e32 v98, s8, v182
	s_cmp_lt_u32 s22, 60
	v_ashrrev_i32_e32 v99, 31, v98
	s_cselect_b64 s[56:57], -1, 0
	s_lshl_b32 s8, s58, 6
	v_lshlrev_b64 v[98:99], 8, v[98:99]
	s_add_i32 s58, s8, 0x100
	s_add_i32 s59, s8, 0xfffff100
	v_lshl_add_u64 v[98:99], s[54:55], 0, v[98:99]
	s_and_b64 s[54:55], s[56:57], exec
	v_lshl_add_u64 v[100:101], v[184:185], 0, s[8:9]
	s_cselect_b32 s8, s58, s59
	v_lshl_add_u64 v[220:221], v[98:99], 0, v[178:179]
	v_add_u32_e32 v98, s8, v182
	v_ashrrev_i32_e32 v99, 31, v98
	s_cselect_b32 s55, s19, s21
	s_cselect_b32 s54, s18, s20
	v_lshlrev_b64 v[98:99], 8, v[98:99]
	v_lshl_add_u64 v[98:99], s[54:55], 0, v[98:99]
	global_load_dwordx2 v[206:207], v[100:101], off offset:256
	v_lshl_add_u64 v[222:223], v[98:99], 0, v[178:179]
	s_waitcnt lgkmcnt(0)
	v_mfma_f32_32x32x64_f8f6f4 v[98:113], v[82:89], v[114:121], 0
	v_exp_f32_e32 v195, v91
	v_exp_f32_e32 v224, v92
	v_exp_f32_e32 v225, v93
	v_exp_f32_e32 v226, v94
	v_exp_f32_e32 v227, v95
	v_exp_f32_e32 v228, v96
	v_exp_f32_e32 v229, v97
	ds_read_b128 v[170:173], v90 offset:5120
	ds_read_b128 v[174:177], v90 offset:5136
	ds_read_b128 v[162:165], v90 offset:7680
	ds_read_b128 v[166:169], v90 offset:7696
	v_pk_add_f32 v[90:91], v[188:189], v[200:201]
	v_pk_add_f32 v[92:93], v[186:187], v[198:199]
	v_pk_add_f32 v[90:91], v[202:203], v[90:91]
	v_pk_add_f32 v[92:93], v[196:197], v[92:93]
	v_pk_add_f32 v[90:91], v[194:195], v[90:91]
	v_pk_add_f32 v[92:93], v[224:225], v[92:93]
	v_exp_f32_e32 v66, v66
	v_exp_f32_e32 v67, v67
	v_exp_f32_e32 v68, v68
	v_exp_f32_e32 v69, v69
	v_exp_f32_e32 v70, v70
	v_exp_f32_e32 v71, v71
	v_exp_f32_e32 v72, v72
	v_pk_add_f32 v[230:231], v[228:229], v[92:93]
	v_pk_add_f32 v[232:233], v[226:227], v[90:91]
	v_mfma_f32_32x32x64_f8f6f4 v[82:97], v[82:89], v[122:129], 0
	v_exp_f32_e32 v73, v73
	v_exp_f32_e32 v74, v74
	v_exp_f32_e32 v75, v75
	v_exp_f32_e32 v76, v76
	v_exp_f32_e32 v77, v77
	v_exp_f32_e32 v78, v78
	v_exp_f32_e32 v79, v79
	v_exp_f32_e32 v80, v80
	v_exp_f32_e32 v81, v81
	v_pk_add_f32 v[188:189], v[192:193], v[66:67]
	v_pk_add_f32 v[190:191], v[190:191], v[68:69]
	v_pk_add_f32 v[188:189], v[70:71], v[188:189]
	v_pk_add_f32 v[190:191], v[72:73], v[190:191]
	v_cvt_scalef32_pk_fp8_f32 v186, v200, v201, s36
	v_pk_add_f32 v[188:189], v[74:75], v[188:189]
	v_pk_add_f32 v[190:191], v[76:77], v[190:191]
	v_cvt_scalef32_pk_fp8_f32 v187, v202, v203, s36
	v_cvt_scalef32_pk_fp8_f32 v186, v198, v199, s36 op_sel:[0,0,0,1]
	v_pk_add_f32 v[192:193], v[78:79], v[188:189]
	v_pk_add_f32 v[190:191], v[80:81], v[190:191]
	v_mfma_f32_32x32x64_f8f6f4 v[2:17], v[154:161], v[130:137], v[2:17]
	s_mulk_i32 s51, 0x2800
	v_cvt_scalef32_pk_fp8_f32 v188, v194, v195, s36
	v_cvt_scalef32_pk_fp8_f32 v189, v226, v227, s36
	v_cvt_scalef32_pk_fp8_f32 v154, v66, v67, s36
	v_cvt_scalef32_pk_fp8_f32 v155, v70, v71, s36
	v_cvt_scalef32_pk_fp8_f32 v156, v74, v75, s36
	v_cvt_scalef32_pk_fp8_f32 v157, v78, v79, s36
	v_cvt_scalef32_pk_fp8_f32 v187, v196, v197, s36 op_sel:[0,0,0,1]
	v_add_u32_e32 v234, s51, v219
	v_cvt_scalef32_pk_fp8_f32 v188, v224, v225, s36 op_sel:[0,0,0,1]
	v_cvt_scalef32_pk_fp8_f32 v189, v228, v229, s36 op_sel:[0,0,0,1]
	v_cvt_scalef32_pk_fp8_f32 v154, v68, v69, s36 op_sel:[0,0,0,1]
	v_cvt_scalef32_pk_fp8_f32 v155, v72, v73, s36 op_sel:[0,0,0,1]
	v_cvt_scalef32_pk_fp8_f32 v156, v76, v77, s36 op_sel:[0,0,0,1]
	v_cvt_scalef32_pk_fp8_f32 v157, v80, v81, s36 op_sel:[0,0,0,1]
	v_exp_f32_e32 v98, v98
	v_exp_f32_e32 v99, v99
	v_mfma_f32_32x32x64_f8f6f4 v[34:49], v[146:153], v[138:145], v[34:49]
	v_exp_f32_e32 v100, v100
	v_exp_f32_e32 v101, v101
	v_exp_f32_e32 v102, v102
	v_exp_f32_e32 v103, v103
	v_exp_f32_e32 v104, v104
	v_exp_f32_e32 v105, v105
	v_exp_f32_e32 v106, v106
	v_exp_f32_e32 v107, v107
	v_exp_f32_e32 v108, v108
	v_exp_f32_e32 v109, v109
	v_exp_f32_e32 v110, v110
	v_exp_f32_e32 v111, v111
	v_exp_f32_e32 v112, v112
	v_exp_f32_e32 v113, v113
	ds_read_b128 v[194:197], v234
	ds_read_b128 v[198:201], v234 offset:16
	v_pk_add_f32 v[66:67], v[232:233], v[98:99]
	v_pk_add_f32 v[68:69], v[230:231], v[100:101]
	v_pk_add_f32 v[66:67], v[102:103], v[66:67]
	v_pk_add_f32 v[68:69], v[104:105], v[68:69]
	v_pk_add_f32 v[66:67], v[106:107], v[66:67]
	v_pk_add_f32 v[68:69], v[108:109], v[68:69]
	v_pk_add_f32 v[140:141], v[110:111], v[66:67]
	v_pk_add_f32 v[138:139], v[112:113], v[68:69]
	v_mfma_f32_32x32x64_f8f6f4 v[18:33], v[146:153], v[130:137], v[18:33]
	v_exp_f32_e32 v82, v82
	v_exp_f32_e32 v83, v83
	v_exp_f32_e32 v84, v84
	v_exp_f32_e32 v85, v85
	v_exp_f32_e32 v86, v86
	v_exp_f32_e32 v87, v87
	v_exp_f32_e32 v88, v88
	v_exp_f32_e32 v89, v89
	v_exp_f32_e32 v90, v90
	v_exp_f32_e32 v91, v91
	v_exp_f32_e32 v92, v92
	v_exp_f32_e32 v93, v93
	v_exp_f32_e32 v94, v94
	v_exp_f32_e32 v95, v95
	v_exp_f32_e32 v96, v96
	v_exp_f32_e32 v97, v97
	v_pk_add_f32 v[66:67], v[192:193], v[82:83]
	v_pk_add_f32 v[68:69], v[190:191], v[84:85]
	v_pk_add_f32 v[66:67], v[86:87], v[66:67]
	v_pk_add_f32 v[68:69], v[88:89], v[68:69]
	v_pk_add_f32 v[130:131], v[90:91], v[66:67]
	v_pk_add_f32 v[132:133], v[92:93], v[68:69]
	s_waitcnt lgkmcnt(0)
; DI void attn_unit_d8(unsigned char* lds, const AttnArgs& a) {
;     ...
;     auto expsum = [&](f32x16& sc, f32x4& l) __attribute__((always_inline)) {
; #pragma unroll
;         for (int i = 0; i < 16; ++i) sc[i] = __builtin_amdgcn_exp2f(sc[i]);
; #pragma unroll
;         for (int i = 0; i < 4; ++i) l += (f32x4){sc[4 * i], sc[4 * i + 1], sc[4 * i + 2], sc[4 * i + 3]};
;     };
;     auto pack8 = [&](const f32x16& s0, const f32x16& s1) __attribute__((always_inline)) -> v8i { v8i p;
; #pragma unroll
;         for (int g = 0; g < 4; ++g) { p[g] = (int)pk4_fp8_div16(s0[4 * g], s0[4 * g + 1], s0[4 * g + 2], s0[4 * g + 3]); p[4 + g] = (int)pk4_fp8_div16(s1[4 * g], s1[4 * g + 1], s1[4 * g + 2], s1[4 * g + 3]); }
;         return p; };
;     auto pack4 = [&](const f32x16& sc, v8i& p, const int o) __attribute__((always_inline)) {
; #pragma unroll
;         for (int g = 0; g < 4; ++g) p[o + g] = (int)pk4_fp8_div16(sc[4 * g], sc[4 * g + 1], sc[4 * g + 2], sc[4 * g + 3]); };
;     auto qk = [&](const unsigned char* Kb, int hh, f32x16& sa, f32x16& sb) __attribute__((always_inline)) { const v8i kf = rd32(Kb + koff + hh * 32 * A8_PITCH);
;         sa = mfma8(kf, qfa, (f32x16){}); sb = mfma8(kf, qfb, (f32x16){}); };
;     gload(a.t0, kreg0, vreg0); gload(a.t0 + 1, kreg1, vreg1); lstore(0, kreg0, vreg0); lstore(1, kreg1, vreg1);
;     gload(a.t0 + 2, kreg0, vreg0); lstore(2, kreg0, vreg0);
;     __syncthreads();
;     asm volatile("" : "+v"(qfa), "+v"(qfb));
;     f32x16 s0a, s0b, s1a, s1b;
;     qk(lds, 0, s0a, s0b);
;     if (wid >= 4) __builtin_amdgcn_s_setprio(1);
;     int sb = 0;
;     const v8i zz8 = (v8i){0, 0, 0, 0, 0, 0, 0, 0};
;     v8i PaX = zz8, PbX = zz8, PaY = zz8, PbY = zz8, vX0 = zz8, vX1 = zz8, vY0 = zz8, vY1 = zz8;
;     auto tile = [&](const unsigned char* Kb, const unsigned char* Kn, v8i& Pa, v8i& Pb, v8i& v0, v8i& v1, const v8i& Qa, const v8i& Qb, const v8i& w0, const v8i& w1) __attribute__((always_inline)) {
;         qk(Kb, 1, s1a, s1b);
;         v0 = rd32(Kb + voff); v1 = rd32(Kb + voff + 32 * A8_PITCH);
;         o0[0] = mfma8(w0, Qa, o0[0]); o1[0] = mfma8(w0, Qb, o1[0]); o0[1] = mfma8(w1, Qa, o0[1]); o1[1] = mfma8(w1, Qb, o1[1]);
;         expsum(s0a, l0); expsum(s0b, l1); pack4(s0a, Pa, 0); pack4(s0b, Pb, 0);
;         qk(Kn, 0, s0a, s0b);
;         expsum(s1a, l0); expsum(s1b, l1); pack4(s1a, Pa, 4); pack4(s1b, Pb, 4);
; #pragma unroll
	v_mfma_f32_32x32x64_f8f6f4 v[66:81], v[194:201], v[114:121], 0
	v_cvt_scalef32_pk_fp8_f32 v190, v98, v99, s36
	v_cvt_scalef32_pk_fp8_f32 v191, v102, v103, s36
	v_cvt_scalef32_pk_fp8_f32 v192, v106, v107, s36
	v_cvt_scalef32_pk_fp8_f32 v193, v110, v111, s36
	v_cvt_scalef32_pk_fp8_f32 v158, v82, v83, s36
	v_cvt_scalef32_pk_fp8_f32 v159, v86, v87, s36
	v_pk_add_f32 v[142:143], v[96:97], v[132:133]
	v_pk_add_f32 v[144:145], v[94:95], v[130:131]
	v_cvt_scalef32_pk_fp8_f32 v160, v90, v91, s36
	v_cvt_scalef32_pk_fp8_f32 v190, v100, v101, s36 op_sel:[0,0,0,1]
	v_cvt_scalef32_pk_fp8_f32 v191, v104, v105, s36 op_sel:[0,0,0,1]
	v_cvt_scalef32_pk_fp8_f32 v192, v108, v109, s36 op_sel:[0,0,0,1]
	v_cvt_scalef32_pk_fp8_f32 v193, v112, v113, s36 op_sel:[0,0,0,1]
	v_cvt_scalef32_pk_fp8_f32 v158, v84, v85, s36 op_sel:[0,0,0,1]
	v_cvt_scalef32_pk_fp8_f32 v159, v88, v89, s36 op_sel:[0,0,0,1]
	v_mfma_f32_32x32x64_f8f6f4 v[98:113], v[194:201], v[122:129], 0
	global_load_dwordx2 v[194:195], v[220:221], off
	global_load_dwordx2 v[196:197], v[222:223], off
	ds_read_b128 v[130:133], v234 offset:2560
	ds_read_b128 v[134:137], v234 offset:2576
	v_exp_f32_e32 v146, v66
	s_add_i32 s80, s61, 0
	v_exp_f32_e32 v147, v67
	s_lshr_b32 s73, s80, 2
	s_mulk_i32 s52, 0x2800
	s_add_i32 s8, s52, 0
	v_cvt_scalef32_pk_fp8_f32 v161, v94, v95, s36
	v_add_u32_e32 v224, s8, v183
	v_cvt_scalef32_pk_fp8_f32 v160, v92, v93, s36 op_sel:[0,0,0,1]
	v_cvt_scalef32_pk_fp8_f32 v161, v96, v97, s36 op_sel:[0,0,0,1]
	v_exp_f32_e32 v148, v68
	s_lshl_b32 s73, s73, 9
	v_exp_f32_e32 v149, v69
	s_add_i32 s73, s73, s46
	v_exp_f32_e32 v150, v70
	s_mul_i32 s75, s73, 0xaaab
	v_exp_f32_e32 v151, v71
	s_lshr_b32 s75, s75, 22
	v_exp_f32_e32 v152, v72
	s_mul_i32 s76, s75, 0x60
	v_exp_f32_e32 v153, v73
	s_sub_i32 s76, s73, s76
	v_exp_f32_e32 v198, v74
	s_lshr_b32 s77, s76, 6
	v_exp_f32_e32 v199, v75
	s_lshl_b32 s78, s77, 6
	v_exp_f32_e32 v200, v76
	s_sub_i32 s76, s76, s78
	v_exp_f32_e32 v201, v77
	s_sub_i32 s78, 3, s77
	v_exp_f32_e32 v202, v78
	s_lshr_b32 s79, s76, s78
	v_exp_f32_e32 v203, v79
	s_lshl_b32 s79, s79, 2
	v_exp_f32_e32 v220, v80
	s_and_b32 s81, s80, 3
	v_exp_f32_e32 v221, v81
	s_add_i32 s79, s79, s81
	v_pk_add_f32 v[66:67], v[140:141], v[146:147]
	s_waitcnt lgkmcnt(0)
	v_mfma_f32_32x32x64_f8f6f4 v[82:97], v[130:137], v[114:121], 0
	v_add_f32_e64 v68, v138, v148
	v_add_f32_e64 v69, v139, v149
	v_add_f32_e64 v66, v150, v66
	v_add_f32_e64 v67, v151, v67
	v_add_f32_e64 v68, v152, v68
	v_add_f32_e64 v69, v153, v69
	v_add_f32_e64 v138, v198, v66
	v_add_f32_e64 v139, v199, v67
	v_add_f32_e64 v140, v200, v68
	v_add_f32_e64 v141, v201, v69
	v_exp_f32_e32 v98, v98
	s_lshl_b32 s79, s79, 5
	v_exp_f32_e32 v99, v99
	s_lshl_b32 s81, s63, 2
	v_exp_f32_e32 v100, v100
	s_add_i32 s81, s81, s79
	v_exp_f32_e32 v101, v101
	s_sub_i32 s78, 13, s77
	v_exp_f32_e32 v102, v102
	s_lshl_b32 s81, s81, s78
	v_exp_f32_e32 v103, v103
	s_lshr_b32 s78, 7, s77
	v_exp_f32_e32 v104, v104
	s_and_b32 s78, s76, s78
	v_exp_f32_e32 v105, v105
	s_lshl_b32 s72, s78, 10
	v_exp_f32_e32 v106, v106
	s_add_i32 s81, s81, s72
	v_exp_f32_e32 v107, v107
	s_add_i32 s72, s75, 32
	v_exp_f32_e32 v108, v108
	s_sub_i32 s80, 23, s77
	v_exp_f32_e32 v109, v109
	s_lshl_b32 s72, s72, s80
	v_exp_f32_e32 v110, v110
	s_add_i32 s81, s81, s72
	v_exp_f32_e32 v111, v111
	s_cmp_eq_u32 s77, 0
	s_cselect_b64 s[84:85], s[66:67], s[68:69]
	v_exp_f32_e32 v112, v112
	s_add_u32 s84, s84, s81
	s_addc_u32 s85, s85, 0
	v_exp_f32_e32 v113, v113
	s_lshr_b32 s80, 0x2000, s77
	v_exp_f32_e32 v82, v82
	s_and_b32 s72, s78, 3
	v_mfma_f32_32x32x64_f8f6f4 v[66:81], v[130:137], v[122:129], 0
	v_add_f32_e64 v130, v144, v98
	v_add_f32_e64 v131, v145, v99
	v_add_f32_e64 v132, v142, v100
	v_add_f32_e64 v133, v143, v101
	v_add_f32_e64 v142, v102, v130
	v_add_f32_e64 v143, v103, v131
	v_add_f32_e64 v132, v104, v132
	v_add_f32_e64 v133, v105, v133
	v_add_f32_e64 v134, v220, v140
	v_add_f32_e64 v135, v221, v141
	v_add_f32_e64 v136, v202, v138
	v_add_f32_e64 v137, v203, v139
	v_pk_add_f32 v[142:143], v[106:107], v[142:143]
	v_pk_add_f32 v[132:133], v[108:109], v[132:133]
	v_cvt_scalef32_pk_fp8_f32 v138, v146, v147, s36
	v_cvt_scalef32_pk_fp8_f32 v139, v150, v151, s36
	v_cvt_scalef32_pk_fp8_f32 v140, v198, v199, s36
	v_cvt_scalef32_pk_fp8_f32 v141, v202, v203, s36
	v_cvt_scalef32_pk_fp8_f32 v130, v98, v99, s36
	v_cvt_scalef32_pk_fp8_f32 v131, v102, v103, s36
	v_pk_add_f32 v[146:147], v[112:113], v[132:133]
	v_pk_add_f32 v[150:151], v[110:111], v[142:143]
	v_mfma_f32_32x32x64_f8f6f4 v[50:65], v[170:177], v[186:193], v[50:65]
	v_exp_f32_e32 v83, v83
	s_lshl_b32 s72, s72, 19
	v_exp_f32_e32 v84, v84
	s_lshr_b32 s81, s78, 2
	v_exp_f32_e32 v85, v85
	s_lshl_b32 s81, s81, 17
; DI void attn_unit_d8(unsigned char* lds, const AttnArgs& a) {
;     ...
;     auto expsum = [&](f32x16& sc, f32x4& l) __attribute__((always_inline)) {
; #pragma unroll
;         for (int i = 0; i < 16; ++i) sc[i] = __builtin_amdgcn_exp2f(sc[i]);
; #pragma unroll
;         for (int i = 0; i < 4; ++i) l += (f32x4){sc[4 * i], sc[4 * i + 1], sc[4 * i + 2], sc[4 * i + 3]};
;     };
;     auto pack8 = [&](const f32x16& s0, const f32x16& s1) __attribute__((always_inline)) -> v8i { v8i p;
; #pragma unroll
;         for (int g = 0; g < 4; ++g) { p[g] = (int)pk4_fp8_div16(s0[4 * g], s0[4 * g + 1], s0[4 * g + 2], s0[4 * g + 3]); p[4 + g] = (int)pk4_fp8_div16(s1[4 * g], s1[4 * g + 1], s1[4 * g + 2], s1[4 * g + 3]); }
;         return p; };
;     auto pack4 = [&](const f32x16& sc, v8i& p, const int o) __attribute__((always_inline)) {
; #pragma unroll
;         for (int g = 0; g < 4; ++g) p[o + g] = (int)pk4_fp8_div16(sc[4 * g], sc[4 * g + 1], sc[4 * g + 2], sc[4 * g + 3]); };
;     auto qk = [&](const unsigned char* Kb, int hh, f32x16& sa, f32x16& sb) __attribute__((always_inline)) { const v8i kf = rd32(Kb + koff + hh * 32 * A8_PITCH);
;         sa = mfma8(kf, qfa, (f32x16){}); sb = mfma8(kf, qfb, (f32x16){}); };
;     gload(a.t0, kreg0, vreg0); gload(a.t0 + 1, kreg1, vreg1); lstore(0, kreg0, vreg0); lstore(1, kreg1, vreg1);
;     gload(a.t0 + 2, kreg0, vreg0); lstore(2, kreg0, vreg0);
;     __syncthreads();
;     asm volatile("" : "+v"(qfa), "+v"(qfb));
;     f32x16 s0a, s0b, s1a, s1b;
;     qk(lds, 0, s0a, s0b);
;     if (wid >= 4) __builtin_amdgcn_s_setprio(1);
;     int sb = 0;
;     const v8i zz8 = (v8i){0, 0, 0, 0, 0, 0, 0, 0};
;     v8i PaX = zz8, PbX = zz8, PaY = zz8, PbY = zz8, vX0 = zz8, vX1 = zz8, vY0 = zz8, vY1 = zz8;
;     auto tile = [&](const unsigned char* Kb, const unsigned char* Kn, v8i& Pa, v8i& Pb, v8i& v0, v8i& v1, const v8i& Qa, const v8i& Qb, const v8i& w0, const v8i& w1) __attribute__((always_inline)) {
;         qk(Kb, 1, s1a, s1b);
;         v0 = rd32(Kb + voff); v1 = rd32(Kb + voff + 32 * A8_PITCH);
;         o0[0] = mfma8(w0, Qa, o0[0]); o1[0] = mfma8(w0, Qb, o1[0]); o0[1] = mfma8(w1, Qa, o0[1]); o1[1] = mfma8(w1, Qb, o1[1]);
;         expsum(s0a, l0); expsum(s0b, l1); pack4(s0a, Pa, 0); pack4(s0b, Pb, 0);
;         qk(Kn, 0, s0a, s0b);
;         expsum(s1a, l0); expsum(s1b, l1); pack4(s1a, Pa, 4); pack4(s1b, Pb, 4);
; #pragma unroll
	v_add_u32_e32 v102, s50, v219
	v_exp_f32_e32 v86, v86
	s_add_i32 s72, s72, s81
	v_exp_f32_e32 v87, v87
	s_lshl_b32 s81, s78, 18
	v_exp_f32_e32 v88, v88
	s_cmp_eq_u32 s77, 0
	s_cselect_b32 s72, s72, s81
	v_exp_f32_e32 v89, v89
	s_mul_i32 s81, s77, 0xc000000
	v_cvt_scalef32_pk_fp8_f32 v130, v100, v101, s36 op_sel:[0,0,0,1]
	v_cvt_scalef32_pk_fp8_f32 v131, v104, v105, s36 op_sel:[0,0,0,1]
	v_exp_f32_e32 v90, v90
	s_add_i32 s81, s81, 0x9094000
	v_exp_f32_e32 v91, v91
	s_add_i32 s72, s72, s79
	v_exp_f32_e32 v92, v92
	s_sub_i32 s73, 21, s77
	v_exp_f32_e32 v93, v93
	s_lshl_b32 s73, s75, s73
	ds_read_b128 v[98:101], v102
	ds_read_b128 v[102:105], v102 offset:16
	v_cvt_scalef32_pk_fp8_f32 v138, v148, v149, s36 op_sel:[0,0,0,1]
	v_cvt_scalef32_pk_fp8_f32 v139, v152, v153, s36 op_sel:[0,0,0,1]
	v_cvt_scalef32_pk_fp8_f32 v140, v200, v201, s36 op_sel:[0,0,0,1]
	v_cvt_scalef32_pk_fp8_f32 v141, v220, v221, s36 op_sel:[0,0,0,1]
	v_exp_f32_e32 v94, v94
	s_add_i32 s72, s72, s73
	v_exp_f32_e32 v95, v95
	s_add_u32 s72, s72, s81
	v_mfma_f32_32x32x64_f8f6f4 v[2:17], v[170:177], v[154:161], v[2:17]
	v_exp_f32_e32 v148, v96
	s_or_b32 s79, s72, s77
	v_cvt_scalef32_pk_fp8_f32 v132, v106, v107, s36
	v_exp_f32_e32 v149, v97
	v_pk_add_f32 v[96:97], v[136:137], v[82:83]
	v_pk_add_f32 v[106:107], v[134:135], v[84:85]
	v_exp_f32_e32 v66, v66
	v_exp_f32_e32 v67, v67
	v_exp_f32_e32 v68, v68
	v_exp_f32_e32 v69, v69
	v_cvt_scalef32_pk_fp8_f32 v133, v110, v111, s36
	v_pk_add_f32 v[106:107], v[88:89], v[106:107]
	v_pk_add_f32 v[96:97], v[86:87], v[96:97]
	v_exp_f32_e32 v70, v70
	v_exp_f32_e32 v71, v71
	v_exp_f32_e32 v72, v72
	v_exp_f32_e32 v73, v73
	v_cvt_scalef32_pk_fp8_f32 v132, v108, v109, s36 op_sel:[0,0,0,1]
	v_cvt_scalef32_pk_fp8_f32 v133, v112, v113, s36 op_sel:[0,0,0,1]
	v_pk_add_f32 v[96:97], v[90:91], v[96:97]
	v_pk_add_f32 v[106:107], v[92:93], v[106:107]
	v_exp_f32_e32 v74, v74
	v_exp_f32_e32 v75, v75
	v_mfma_f32_32x32x64_f8f6f4 v[34:49], v[162:169], v[186:193], v[34:49]
	v_exp_f32_e32 v76, v76
	v_exp_f32_e32 v77, v77
	v_exp_f32_e32 v78, v78
	v_exp_f32_e32 v79, v79
	v_exp_f32_e32 v80, v80
	v_exp_f32_e32 v81, v81
	v_cvt_scalef32_pk_fp8_f32 v142, v82, v83, s36
	v_cvt_scalef32_pk_fp8_f32 v143, v86, v87, s36
	v_cvt_scalef32_pk_fp8_f32 v144, v90, v91, s36
	v_cvt_scalef32_pk_fp8_f32 v142, v84, v85, s36 op_sel:[0,0,0,1]
	v_pk_add_f32 v[82:83], v[150:151], v[66:67]
	v_pk_add_f32 v[84:85], v[146:147], v[68:69]
	s_mulk_i32 s53, 0x2800
	v_pk_add_f32 v[186:187], v[148:149], v[106:107]
	v_pk_add_f32 v[188:189], v[94:95], v[96:97]
	v_cvt_scalef32_pk_fp8_f32 v145, v94, v95, s36
	v_cvt_scalef32_pk_fp8_f32 v143, v88, v89, s36 op_sel:[0,0,0,1]
	v_cvt_scalef32_pk_fp8_f32 v144, v92, v93, s36 op_sel:[0,0,0,1]
	v_pk_add_f32 v[84:85], v[72:73], v[84:85]
	v_mfma_f32_32x32x64_f8f6f4 v[18:33], v[162:169], v[154:161], v[18:33]
	v_add_f32_e64 v82, v70, v82
	v_add_f32_e64 v83, v71, v83
	s_add_i32 s51, s53, 0
	v_add_f32_e64 v82, v74, v82
	v_add_f32_e64 v83, v75, v83
	v_add_f32_e64 v84, v76, v84
	v_add_f32_e64 v85, v77, v85
	v_cvt_scalef32_pk_fp8_f32 v134, v66, v67, s36
	v_cvt_scalef32_pk_fp8_f32 v135, v70, v71, s36
	v_cvt_scalef32_pk_fp8_f32 v136, v74, v75, s36
	v_cvt_scalef32_pk_fp8_f32 v137, v78, v79, s36
	v_pk_add_f32 v[190:191], v[80:81], v[84:85]
	v_pk_add_f32 v[192:193], v[78:79], v[82:83]
	v_add_u32_e32 v106, s8, v218
	v_add_u32_e32 v107, s51, v183
	v_cvt_scalef32_pk_fp8_f32 v145, v148, v149, s36 op_sel:[0,0,0,1]
	v_cvt_scalef32_pk_fp8_f32 v134, v68, v69, s36 op_sel:[0,0,0,1]
	v_cvt_scalef32_pk_fp8_f32 v135, v72, v73, s36 op_sel:[0,0,0,1]
	v_cvt_scalef32_pk_fp8_f32 v136, v76, v77, s36 op_sel:[0,0,0,1]
	v_cvt_scalef32_pk_fp8_f32 v137, v80, v81, s36 op_sel:[0,0,0,1]
	s_waitcnt lgkmcnt(0)
	v_mfma_f32_32x32x64_f8f6f4 v[82:97], v[98:105], v[114:121], 0
	ds_read_b128 v[154:157], v234 offset:5120
	ds_read_b128 v[158:161], v234 offset:5136
	ds_read_b128 v[146:149], v234 offset:7680
	ds_read_b128 v[150:153], v234 offset:7696
	s_cmpk_gt_i32 s46, 0x1ff
	s_cbranch_scc1 .Lmy_rd1_ldum
	s_add_i32 s72, s61, -1
	s_cmp_lt_u32 s72, 24
	s_cbranch_scc0 .Lmy_rd1_noc
	s_waitcnt vmcnt(4)
	v_cvt_scalef32_pk_fp8_f32 v236, v236, v240, s62
	v_cvt_scalef32_pk_fp8_f32 v237, v237, v241, s62
	v_cvt_scalef32_pk_fp8_f32 v238, v238, v242, s62
	v_cvt_scalef32_pk_fp8_f32 v239, v239, v243, s62
	v_cvt_scalef32_pk_fp8_f32 v236, v244, v248, s62 op_sel:[0,0,0,1]
	v_cvt_scalef32_pk_fp8_f32 v237, v245, v249, s62 op_sel:[0,0,0,1]
	v_cvt_scalef32_pk_fp8_f32 v238, v246, v250, s62 op_sel:[0,0,0,1]
	v_cvt_scalef32_pk_fp8_f32 v239, v247, v251, s62 op_sel:[0,0,0,1]
	ds_write_b32 v252, v236
	ds_write_b32 v252, v237 offset:36
	ds_write_b32 v252, v238 offset:72
	ds_write_b32 v252, v239 offset:108

; DI void attn_unit_a8(unsigned char* lds, const AttnArgs& a) {
;     ...
;     auto expsum = [&](f32x16& sc) __attribute__((always_inline)) {
; #pragma unroll
;         for (int i = 0; i < 16; ++i) sc[i] = __builtin_amdgcn_exp2f(sc[i]);
; #pragma unroll
;         for (int i = 0; i < 4; ++i) l0 += (f32x4){sc[4 * i], sc[4 * i + 1], sc[4 * i + 2], sc[4 * i + 3]};
;     };
;     auto pack8 = [&](const f32x16& s0, const f32x16& s1) __attribute__((always_inline)) -> v8i { v8i p;
; #pragma unroll
;         for (int g = 0; g < 4; ++g) { p[g] = (int)pk4_fp8_div16(s0[4 * g], s0[4 * g + 1], s0[4 * g + 2], s0[4 * g + 3]); p[4 + g] = (int)pk4_fp8_div16(s1[4 * g], s1[4 * g + 1], s1[4 * g + 2], s1[4 * g + 3]); }
;         return p; };
;     f32x4 wq[4];
;     const int wn4 = (tid & 63) * 4;
;     constexpr int WPITCH = 36;
;     auto w_decode = [&](int j, const float*& src, unsigned char*& dst, int& ld, int& n0, int& k0, bool& gu) __attribute__((always_inline)) {
;         const int g = (j >> 2) * 512 + a.wl, e = g / 96, rr = g - e * 96; KParamsPtr kp = kparams();
;         if (rr < 64) { src = kp->w_gu + ((size_t)a.wli * NE + e) * (1024 * 2048); dst = kp->ws + WS_WGU + (size_t)a.wli * SZ_WGU + (size_t)e * 2048 * 1024; ld = 2048; n0 = (rr & 7) * 256; k0 = ((rr >> 3) * 4 + (j & 3)) * 32; gu = true; }
;         else { const int q = rr - 64; src = kp->w_dn + ((size_t)a.wli * NE + e) * (1024 * 1024); dst = kp->ws + WS_WDN + (size_t)a.wli * SZ_WDN + (size_t)e * 1024 * 1024; ld = 1024; n0 = (q & 3) * 256; k0 = ((q >> 2) * 4 + (j & 3)) * 32; gu = false; } };
;     auto w_issue = [&](int j) __attribute__((always_inline)) { const float* src; unsigned char* dst; int ld, n0, k0; bool gu; w_decode(j, src, dst, ld, n0, k0, gu);
;         const float* p = src + (size_t)(k0 + 4 * wid) * ld + n0 + wn4;
;         wq[0] = __builtin_nontemporal_load((const f32x4*)p); wq[1] = __builtin_nontemporal_load((const f32x4*)(p + ld));
;         wq[2] = __builtin_nontemporal_load((const f32x4*)(p + (size_t)2 * ld)); wq[3] = __builtin_nontemporal_load((const f32x4*)(p + (size_t)3 * ld)); };
;     auto w_cvt = [&]() __attribute__((always_inline)) { unsigned char* t8 = lds + AT_WT + wn4 * WPITCH + 4 * wid;
; #pragma unroll
;         for (int j = 0; j < 4; ++j) *(unsigned*)(t8 + j * WPITCH) = pk4_fp8_mul64(wq[0][j], wq[1][j], wq[2][j], wq[3][j]); };
;     const int wcol = tid >> 1, whalf = tid & 1;
.LBB0_1934:
	s_min_u32 s8, s50, 64
	s_cmp_lt_u32 s50, 61
	s_cselect_b64 s[10:11], -1, 0
	s_lshl_b32 s8, s8, 6
	s_add_i32 s15, s8, 0xc0
	s_add_i32 s18, s8, 0xfffff0c0
	s_and_b64 s[16:17], s[10:11], exec
	s_cselect_b32 s15, s15, s18
	s_mov_b32 s18, s14
	s_add_i32 s14, s14, 1
	s_cmp_lg_u32 s18, 2
	s_cselect_b32 s14, s14, 0
	s_mul_i32 s19, s14, 0x4680
	v_add_u32_e32 v106, s19, v169
	ds_read_b128 v[50:53], v106
	ds_read_b128 v[54:57], v106 offset:16
	v_add_u32_e32 v58, s15, v130
	s_and_b64 s[10:11], s[10:11], exec
	v_ashrrev_i32_e32 v59, 31, v58
	s_cselect_b32 s16, s42, s12
	s_cselect_b32 s17, s43, s13
	s_waitcnt lgkmcnt(0)
	v_mfma_f32_32x32x64_f8f6f4 v[34:49], v[50:57], v[98:105], 0
	v_lshlrev_b64 v[50:51], 7, v[58:59]
	v_lshl_add_u64 v[50:51], s[16:17], 0, v[50:51]
	v_lshl_add_u64 v[50:51], v[50:51], 0, v[132:133]
	v_lshl_add_u64 v[58:59], v[134:135], 0, s[8:9]
	global_load_dwordx2 v[112:113], v[50:51], off
	ds_read_b128 v[50:53], v106 offset:2560
	ds_read_b128 v[54:57], v106 offset:2576
	global_load_dwordx2 v[114:115], v[58:59], off offset:192
	s_mulk_i32 s18, 0x4680
	v_add_u32_e32 v58, s18, v169
	v_exp_f32_e32 v82, v82
	v_exp_f32_e32 v83, v83
	v_exp_f32_e32 v86, v86
	v_exp_f32_e32 v87, v87
	v_exp_f32_e32 v90, v90
	v_exp_f32_e32 v91, v91
	v_exp_f32_e32 v94, v94
	v_exp_f32_e32 v95, v95
	v_exp_f32_e32 v124, v66
	v_exp_f32_e32 v125, v67
	v_exp_f32_e32 v148, v70
	v_exp_f32_e32 v149, v71
	v_exp_f32_e32 v74, v74
	v_exp_f32_e32 v75, v75
	v_exp_f32_e32 v78, v78
	v_exp_f32_e32 v79, v79
	ds_read_b128 v[116:119], v58 offset:5120
	ds_read_b128 v[120:123], v58 offset:5136
	ds_read_b128 v[140:143], v58 offset:7680
	ds_read_b128 v[144:147], v58 offset:7696
	v_exp_f32_e32 v84, v84
	v_exp_f32_e32 v85, v85
	v_exp_f32_e32 v88, v88
	v_exp_f32_e32 v89, v89
	v_exp_f32_e32 v92, v92
	v_exp_f32_e32 v93, v93
	v_exp_f32_e32 v96, v96
	v_exp_f32_e32 v97, v97
	v_exp_f32_e32 v126, v68
	v_exp_f32_e32 v127, v69
	v_exp_f32_e32 v150, v72
	v_exp_f32_e32 v151, v73
	v_exp_f32_e32 v76, v76
	v_exp_f32_e32 v77, v77
	v_exp_f32_e32 v80, v80
	v_exp_f32_e32 v81, v81
	v_cvt_scalef32_pk_fp8_f32 v66, v82, v83, s69
	v_cvt_scalef32_pk_fp8_f32 v70, v124, v125, s69
	v_cvt_scalef32_pk_fp8_f32 v67, v86, v87, s69
	v_cvt_scalef32_pk_fp8_f32 v71, v148, v149, s69
	v_cvt_scalef32_pk_fp8_f32 v68, v90, v91, s69
	v_cvt_scalef32_pk_fp8_f32 v72, v74, v75, s69
	v_cvt_scalef32_pk_fp8_f32 v69, v94, v95, s69
	v_cvt_scalef32_pk_fp8_f32 v73, v78, v79, s69
	v_cvt_scalef32_pk_fp8_f32 v66, v84, v85, s69 op_sel:[0,0,0,1]
	v_cvt_scalef32_pk_fp8_f32 v70, v126, v127, s69 op_sel:[0,0,0,1]
	v_cvt_scalef32_pk_fp8_f32 v67, v88, v89, s69 op_sel:[0,0,0,1]
	v_cvt_scalef32_pk_fp8_f32 v71, v150, v151, s69 op_sel:[0,0,0,1]
	v_cvt_scalef32_pk_fp8_f32 v68, v92, v93, s69 op_sel:[0,0,0,1]
	v_cvt_scalef32_pk_fp8_f32 v72, v76, v77, s69 op_sel:[0,0,0,1]
	v_cvt_scalef32_pk_fp8_f32 v69, v96, v97, s69 op_sel:[0,0,0,1]
	v_cvt_scalef32_pk_fp8_f32 v73, v80, v81, s69 op_sel:[0,0,0,1]
	s_waitcnt lgkmcnt(4)
	v_mfma_f32_32x32x64_f8f6f4 v[50:65], v[50:57], v[98:105], 0
	s_add_i32 s15, s19, 0x4680
	s_cmp_eq_u32 s14, 2
	v_add_f32_e64 v110, v110, v84
	v_add_f32_e64 v111, v111, v85
	v_add_f32_e64 v82, v108, v82
	v_add_f32_e64 v83, v109, v83
	s_cselect_b64 s[10:11], -1, 0
	v_add_f32_e64 v84, v88, v110
	v_add_f32_e64 v85, v89, v111
	v_add_f32_e64 v82, v86, v82
	v_add_f32_e64 v83, v87, v83
	v_add_f32_e64 v84, v92, v84
	v_add_f32_e64 v85, v93, v85
	v_pk_add_f32 v[82:83], v[90:91], v[82:83]
	s_and_b64 s[16:17], s[10:11], exec
	v_pk_add_f32 v[84:85], v[96:97], v[84:85]
	v_pk_add_f32 v[82:83], v[94:95], v[82:83]
	s_cselect_b32 s8, 0, s15
	v_pk_add_f32 v[82:83], v[124:125], v[82:83]
	v_pk_add_f32 v[84:85], v[126:127], v[84:85]
	s_waitcnt lgkmcnt(2)
	v_mfma_f32_32x32x64_f8f6f4 v[18:33], v[116:123], v[66:73], v[18:33]
	s_add_i32 s8, s8, 0
	v_add_f32_e64 v84, v150, v84
	v_add_f32_e64 v85, v151, v85
	v_add_f32_e64 v82, v148, v82
	v_add_f32_e64 v83, v149, v83
	v_add_f32_e64 v76, v76, v84
	v_add_f32_e64 v77, v77, v85
	v_add_f32_e64 v74, v74, v82
	v_add_f32_e64 v75, v75, v83
	v_add_f32_e64 v110, v80, v76
	v_add_f32_e64 v111, v81, v77
	v_add_f32_e64 v108, v78, v74
	v_add_f32_e64 v109, v79, v75
	s_cmpk_gt_u32 s50, 0x42
	s_waitcnt lgkmcnt(0)
	v_mfma_f32_32x32x64_f8f6f4 v[2:17], v[140:147], v[66:73], v[2:17]
	v_add_u32_e32 v66, s8, v131
	s_waitcnt vmcnt(3)
	ds_write_b64 v66, v[136:137]
	v_add_u32_e32 v66, s8, v168
	v_add_u32_e32 v66, 0x1400, v66
	s_waitcnt vmcnt(2)
	ds_write2_b32 v66, v138, v139 offset1:8
	s_waitcnt lgkmcnt(0)
	s_barrier
; DI void attn_unit_a8(unsigned char* lds, const AttnArgs& a) {
;     ...
;     auto expsum = [&](f32x16& sc) __attribute__((always_inline)) {
; #pragma unroll
;         for (int i = 0; i < 16; ++i) sc[i] = __builtin_amdgcn_exp2f(sc[i]);
; #pragma unroll
;         for (int i = 0; i < 4; ++i) l0 += (f32x4){sc[4 * i], sc[4 * i + 1], sc[4 * i + 2], sc[4 * i + 3]};
;     };
;     auto pack8 = [&](const f32x16& s0, const f32x16& s1) __attribute__((always_inline)) -> v8i { v8i p;
; #pragma unroll
;         for (int g = 0; g < 4; ++g) { p[g] = (int)pk4_fp8_div16(s0[4 * g], s0[4 * g + 1], s0[4 * g + 2], s0[4 * g + 3]); p[4 + g] = (int)pk4_fp8_div16(s1[4 * g], s1[4 * g + 1], s1[4 * g + 2], s1[4 * g + 3]); }
;         return p; };
;     f32x4 wq[4];
;     const int wn4 = (tid & 63) * 4;
;     constexpr int WPITCH = 36;
;     auto w_decode = [&](int j, const float*& src, unsigned char*& dst, int& ld, int& n0, int& k0, bool& gu) __attribute__((always_inline)) {
;         const int g = (j >> 2) * 512 + a.wl, e = g / 96, rr = g - e * 96; KParamsPtr kp = kparams();
;         if (rr < 64) { src = kp->w_gu + ((size_t)a.wli * NE + e) * (1024 * 2048); dst = kp->ws + WS_WGU + (size_t)a.wli * SZ_WGU + (size_t)e * 2048 * 1024; ld = 2048; n0 = (rr & 7) * 256; k0 = ((rr >> 3) * 4 + (j & 3)) * 32; gu = true; }
;         else { const int q = rr - 64; src = kp->w_dn + ((size_t)a.wli * NE + e) * (1024 * 1024); dst = kp->ws + WS_WDN + (size_t)a.wli * SZ_WDN + (size_t)e * 1024 * 1024; ld = 1024; n0 = (q & 3) * 256; k0 = ((q >> 2) * 4 + (j & 3)) * 32; gu = false; } };
;     auto w_issue = [&](int j) __attribute__((always_inline)) { const float* src; unsigned char* dst; int ld, n0, k0; bool gu; w_decode(j, src, dst, ld, n0, k0, gu);
;         const float* p = src + (size_t)(k0 + 4 * wid) * ld + n0 + wn4;
;         wq[0] = __builtin_nontemporal_load((const f32x4*)p); wq[1] = __builtin_nontemporal_load((const f32x4*)(p + ld));
;         wq[2] = __builtin_nontemporal_load((const f32x4*)(p + (size_t)2 * ld)); wq[3] = __builtin_nontemporal_load((const f32x4*)(p + (size_t)3 * ld)); };
;     auto w_cvt = [&]() __attribute__((always_inline)) { unsigned char* t8 = lds + AT_WT + wn4 * WPITCH + 4 * wid;
; #pragma unroll
;         for (int j = 0; j < 4; ++j) *(unsigned*)(t8 + j * WPITCH) = pk4_fp8_mul64(wq[0][j], wq[1][j], wq[2][j], wq[3][j]); };
;     const int wcol = tid >> 1, whalf = tid & 1;
	s_cbranch_scc1 .LBB0_1936
	s_min_u32 s8, s50, 63
	s_cmp_lt_u32 s50, 60
	s_cselect_b64 s[16:17], -1, 0
	s_lshl_b32 s8, s8, 6
	s_add_i32 s15, s8, 0x100
	s_add_i32 s20, s8, 0xfffff100
	s_and_b64 s[18:19], s[16:17], exec
	s_cselect_b32 s15, s15, s20
	s_add_i32 s14, s14, 1
	s_and_b64 s[10:11], s[10:11], exec
	v_add_u32_e32 v82, s15, v130
	s_cselect_b32 s14, 0, s14
	s_and_b64 s[16:17], s[16:17], exec
	v_ashrrev_i32_e32 v83, 31, v82
	s_cselect_b32 s17, s43, s13
	s_cselect_b32 s16, s42, s12
	v_lshlrev_b64 v[82:83], 7, v[82:83]
	s_mul_i32 s10, s14, 0x4680
	v_lshl_add_u64 v[90:91], s[16:17], 0, v[82:83]
	v_add_u32_e32 v86, s10, v169
	v_lshl_add_u64 v[90:91], v[90:91], 0, v[132:133]
	ds_read_b128 v[66:69], v86 offset:2560
	ds_read_b128 v[70:73], v86 offset:2576
	ds_read_b128 v[82:85], v86
	ds_read_b128 v[86:89], v86 offset:16
	global_load_dwordx2 v[136:137], v[90:91], off
	v_lshl_add_u64 v[90:91], v[134:135], 0, s[8:9]
	global_load_dwordx2 v[138:139], v[90:91], off offset:256
	v_exp_f32_e32 v124, v34
	v_exp_f32_e32 v125, v35
	v_exp_f32_e32 v36, v36
	v_exp_f32_e32 v37, v37
	v_exp_f32_e32 v126, v38
	v_exp_f32_e32 v127, v39
	v_exp_f32_e32 v42, v42
	v_exp_f32_e32 v43, v43
	v_exp_f32_e32 v46, v46
	v_exp_f32_e32 v47, v47
	v_exp_f32_e32 v50, v50
	v_exp_f32_e32 v51, v51
	v_exp_f32_e32 v54, v54
	v_exp_f32_e32 v55, v55
	v_exp_f32_e32 v58, v58
	v_exp_f32_e32 v59, v59
	v_exp_f32_e32 v62, v62
	v_exp_f32_e32 v63, v63
	ds_read_b128 v[116:119], v106 offset:5120
	ds_read_b128 v[120:123], v106 offset:5136
	ds_read_b128 v[140:143], v106 offset:7680
	ds_read_b128 v[144:147], v106 offset:7696
	v_exp_f32_e32 v148, v40
	v_exp_f32_e32 v149, v41
	v_exp_f32_e32 v44, v44
	v_exp_f32_e32 v45, v45
	v_exp_f32_e32 v48, v48
	v_exp_f32_e32 v49, v49
	v_exp_f32_e32 v52, v52
	v_exp_f32_e32 v53, v53
	v_exp_f32_e32 v56, v56
	v_exp_f32_e32 v57, v57
	v_exp_f32_e32 v60, v60
	v_exp_f32_e32 v61, v61
	v_exp_f32_e32 v64, v64
	v_exp_f32_e32 v65, v65
	v_cvt_scalef32_pk_fp8_f32 v34, v124, v125, s69
	v_pk_add_f32 v[110:111], v[110:111], v[36:37]
	v_cvt_scalef32_pk_fp8_f32 v34, v36, v37, s69 op_sel:[0,0,0,1]
	s_waitcnt lgkmcnt(6)
	v_mfma_f32_32x32x64_f8f6f4 v[66:81], v[66:73], v[98:105], 0
	v_cvt_scalef32_pk_fp8_f32 v38, v50, v51, s69
	v_cvt_scalef32_pk_fp8_f32 v35, v126, v127, s69
	v_cvt_scalef32_pk_fp8_f32 v39, v54, v55, s69
	v_cvt_scalef32_pk_fp8_f32 v36, v42, v43, s69
	v_cvt_scalef32_pk_fp8_f32 v40, v58, v59, s69
	v_cvt_scalef32_pk_fp8_f32 v37, v46, v47, s69
	v_cvt_scalef32_pk_fp8_f32 v41, v62, v63, s69
	v_cvt_scalef32_pk_fp8_f32 v38, v52, v53, s69 op_sel:[0,0,0,1]
	v_cvt_scalef32_pk_fp8_f32 v35, v148, v149, s69 op_sel:[0,0,0,1]
	v_cvt_scalef32_pk_fp8_f32 v39, v56, v57, s69 op_sel:[0,0,0,1]
	v_cvt_scalef32_pk_fp8_f32 v36, v44, v45, s69 op_sel:[0,0,0,1]
	v_cvt_scalef32_pk_fp8_f32 v40, v60, v61, s69 op_sel:[0,0,0,1]
	v_cvt_scalef32_pk_fp8_f32 v37, v48, v49, s69 op_sel:[0,0,0,1]
	v_cvt_scalef32_pk_fp8_f32 v41, v64, v65, s69 op_sel:[0,0,0,1]
	v_pk_add_f32 v[108:109], v[108:109], v[124:125]
	s_waitcnt lgkmcnt(4)
	v_mfma_f32_32x32x64_f8f6f4 v[82:97], v[82:89], v[98:105], 0
	s_addk_i32 s10, 0x4680
	v_add_f32_e64 v110, v148, v110
	v_add_f32_e64 v111, v149, v111
	v_add_f32_e64 v108, v126, v108
	v_add_f32_e64 v109, v127, v109
	s_cmp_lg_u32 s14, 2
	v_add_f32_e64 v42, v42, v108
	v_add_f32_e64 v43, v43, v109
	v_add_f32_e64 v44, v44, v110
	v_add_f32_e64 v45, v45, v111
	s_cselect_b32 s8, s10, 0
	v_add_f32_e64 v44, v48, v44
	v_add_f32_e64 v45, v49, v45
	v_pk_add_f32 v[42:43], v[46:47], v[42:43]
	s_add_i32 s8, s8, 0
	v_pk_add_f32 v[42:43], v[50:51], v[42:43]
	v_pk_add_f32 v[44:45], v[52:53], v[44:45]
	v_pk_add_f32 v[42:43], v[54:55], v[42:43]
	v_pk_add_f32 v[44:45], v[56:57], v[44:45]
	v_pk_add_f32 v[42:43], v[58:59], v[42:43]
	s_waitcnt lgkmcnt(2)
	v_mfma_f32_32x32x64_f8f6f4 v[18:33], v[116:123], v[34:41], v[18:33]
	v_add_f32_e64 v44, v60, v44
	v_add_f32_e64 v45, v61, v45
	v_add_f32_e64 v108, v62, v42
	v_add_f32_e64 v109, v63, v43
	v_add_f32_e64 v110, v64, v44
	v_add_f32_e64 v111, v65, v45
	s_waitcnt lgkmcnt(0)
	v_mfma_f32_32x32x64_f8f6f4 v[2:17], v[140:147], v[34:41], v[2:17]
	v_add_u32_e32 v34, s8, v131
	s_waitcnt vmcnt(3)
	ds_write_b64 v34, v[112:113]
	v_add_u32_e32 v34, s8, v168
	v_add_u32_e32 v34, 0x1400, v34
	s_waitcnt vmcnt(2)
	ds_write2_b32 v34, v114, v115 offset1:8
	s_waitcnt lgkmcnt(0)
	s_barrier
